# MFMA chain order snake (every consecutive chain shares an A or B fragment pair) on top of holdA4 build
# speedup vs baseline: 1.0266x; 1.0031x over previous
.LBB0_130:
	ds_read_b128 v[144:147], v140
	ds_read_b128 v[148:151], v140 offset:1024
	ds_read_b128 v[152:155], v140 offset:2048
	ds_read_b128 v[156:159], v140 offset:3072
	ds_read_b128 v[164:167], v141
	ds_read_b128 v[168:171], v141 offset:1024
	ds_read_b128 v[172:175], v141 offset:2048
	ds_read_b128 v[176:179], v141 offset:3072
	s_add_u32 s31, s10, 0xfff7c080
	s_addc_u32 s53, s11, -1
	s_cmp_eq_u32 s30, 28
	s_cselect_b32 s55, s25, s53
	s_cselect_b32 s54, s24, s31
	s_cselect_b32 s57, s4, s29
	s_cselect_b32 s56, s5, s28
	s_mov_b32 m0, s23
	ds_read_b128 v[180:183], v163
	ds_read_b128 v[190:193], v163 offset:1024
	ds_read_b128 v[194:197], v163 offset:2048
	ds_read_b128 v[198:201], v163 offset:3072
	ds_read_b128 v[202:205], v163 offset:4096
	ds_read_b128 v[206:209], v163 offset:5120
	ds_read_b128 v[216:219], v163 offset:6144
	ds_read_b128 v[220:223], v163 offset:7168
	global_load_lds_dwordx4 v138, s[10:11]
	s_mov_b32 m0, s33
	s_nop 0
	s_add_u32 s70, s10, s96
	s_addc_u32 s71, s11, s97
	global_load_lds_dwordx4 v138, s[70:71]
	s_waitcnt vmcnt(8)
	s_waitcnt lgkmcnt(0)
	s_barrier
	v_mfma_f32_16x16x32_bf16 v[120:123], v[144:147], v[180:183], v[120:123]
	v_mfma_f32_16x16x32_bf16 v[120:123], v[148:151], v[190:193], v[120:123]
	v_mfma_f32_16x16x32_bf16 v[116:119], v[152:155], v[180:183], v[116:119]
	v_mfma_f32_16x16x32_bf16 v[116:119], v[156:159], v[190:193], v[116:119]
	v_mfma_f32_16x16x32_bf16 v[128:131], v[164:167], v[180:183], v[128:131]
	v_mfma_f32_16x16x32_bf16 v[128:131], v[168:171], v[190:193], v[128:131]
	v_mfma_f32_16x16x32_bf16 v[124:127], v[172:175], v[180:183], v[124:127]
	v_mfma_f32_16x16x32_bf16 v[124:127], v[176:179], v[190:193], v[124:127]
	v_mfma_f32_16x16x32_bf16 v[108:111], v[172:175], v[194:197], v[108:111]
	v_mfma_f32_16x16x32_bf16 v[108:111], v[176:179], v[198:201], v[108:111]
	v_mfma_f32_16x16x32_bf16 v[112:115], v[164:167], v[194:197], v[112:115]
	v_mfma_f32_16x16x32_bf16 v[112:115], v[168:171], v[198:201], v[112:115]
	v_mfma_f32_16x16x32_bf16 v[100:103], v[152:155], v[194:197], v[100:103]
	v_mfma_f32_16x16x32_bf16 v[100:103], v[156:159], v[198:201], v[100:103]
	v_mfma_f32_16x16x32_bf16 v[104:107], v[144:147], v[194:197], v[104:107]
	v_mfma_f32_16x16x32_bf16 v[104:107], v[148:151], v[198:201], v[104:107]
	v_mfma_f32_16x16x32_bf16 v[88:91], v[144:147], v[202:205], v[88:91]
	v_mfma_f32_16x16x32_bf16 v[88:91], v[148:151], v[206:209], v[88:91]
	v_mfma_f32_16x16x32_bf16 v[84:87], v[152:155], v[202:205], v[84:87]
	v_mfma_f32_16x16x32_bf16 v[84:87], v[156:159], v[206:209], v[84:87]
	v_mfma_f32_16x16x32_bf16 v[96:99], v[164:167], v[202:205], v[96:99]
	v_mfma_f32_16x16x32_bf16 v[96:99], v[168:171], v[206:209], v[96:99]
	v_mfma_f32_16x16x32_bf16 v[92:95], v[172:175], v[202:205], v[92:95]
	v_mfma_f32_16x16x32_bf16 v[92:95], v[176:179], v[206:209], v[92:95]
	v_mfma_f32_16x16x32_bf16 v[76:79], v[172:175], v[216:219], v[76:79]
	v_mfma_f32_16x16x32_bf16 v[76:79], v[176:179], v[220:223], v[76:79]
	v_mfma_f32_16x16x32_bf16 v[80:83], v[164:167], v[216:219], v[80:83]
	v_mfma_f32_16x16x32_bf16 v[80:83], v[168:171], v[220:223], v[80:83]
	v_mfma_f32_16x16x32_bf16 v[68:71], v[152:155], v[216:219], v[68:71]
	v_mfma_f32_16x16x32_bf16 v[68:71], v[156:159], v[220:223], v[68:71]
	v_mfma_f32_16x16x32_bf16 v[72:75], v[144:147], v[216:219], v[72:75]
	v_mfma_f32_16x16x32_bf16 v[72:75], v[148:151], v[220:223], v[72:75]
	s_barrier
	s_mov_b32 m0, s45
	ds_read_b128 v[180:183], v163 offset:16384
	ds_read_b128 v[190:193], v163 offset:17408
	ds_read_b128 v[194:197], v163 offset:18432
	ds_read_b128 v[198:201], v163 offset:19456
	ds_read_b128 v[202:205], v163 offset:20480
	ds_read_b128 v[206:209], v163 offset:21504
	ds_read_b128 v[216:219], v163 offset:22528
	ds_read_b128 v[220:223], v163 offset:23552
	global_load_lds_dwordx4 v132, s[56:57]
	s_mov_b32 m0, s46
	s_nop 0
	s_add_u32 s70, s56, s90
	s_addc_u32 s71, s57, s91
	global_load_lds_dwordx4 v132, s[70:71]
	s_mov_b32 m0, s47
	s_nop 0
	s_add_u32 s70, s56, s60
	s_addc_u32 s71, s57, s61
	global_load_lds_dwordx4 v132, s[70:71]
	s_mov_b32 m0, s48
	s_nop 0
	s_add_u32 s70, s56, s64
	s_addc_u32 s71, s57, s65
	global_load_lds_dwordx4 v132, s[70:71]
	s_mov_b32 m0, s37
	s_nop 0
	global_load_lds_dwordx4 v134, s[54:55]
	s_mov_b32 m0, s38
	s_nop 0
	s_add_u32 s70, s54, s96
	s_addc_u32 s71, s55, s97
	global_load_lds_dwordx4 v134, s[70:71]
	s_waitcnt vmcnt(8)
	s_waitcnt lgkmcnt(0)
	s_barrier
	v_mfma_f32_16x16x32_bf16 v[56:59], v[144:147], v[180:183], v[56:59]
	v_mfma_f32_16x16x32_bf16 v[56:59], v[148:151], v[190:193], v[56:59]
	v_mfma_f32_16x16x32_bf16 v[52:55], v[152:155], v[180:183], v[52:55]
	v_mfma_f32_16x16x32_bf16 v[52:55], v[156:159], v[190:193], v[52:55]
	v_mfma_f32_16x16x32_bf16 v[64:67], v[164:167], v[180:183], v[64:67]
	v_mfma_f32_16x16x32_bf16 v[64:67], v[168:171], v[190:193], v[64:67]
	v_mfma_f32_16x16x32_bf16 v[60:63], v[172:175], v[180:183], v[60:63]
	v_mfma_f32_16x16x32_bf16 v[60:63], v[176:179], v[190:193], v[60:63]
	v_mfma_f32_16x16x32_bf16 v[44:47], v[172:175], v[194:197], v[44:47]
	v_mfma_f32_16x16x32_bf16 v[44:47], v[176:179], v[198:201], v[44:47]
	v_mfma_f32_16x16x32_bf16 v[48:51], v[164:167], v[194:197], v[48:51]
	v_mfma_f32_16x16x32_bf16 v[48:51], v[168:171], v[198:201], v[48:51]
	v_mfma_f32_16x16x32_bf16 v[36:39], v[152:155], v[194:197], v[36:39]
	v_mfma_f32_16x16x32_bf16 v[36:39], v[156:159], v[198:201], v[36:39]
	v_mfma_f32_16x16x32_bf16 v[40:43], v[144:147], v[194:197], v[40:43]
	v_mfma_f32_16x16x32_bf16 v[40:43], v[148:151], v[198:201], v[40:43]
	v_mfma_f32_16x16x32_bf16 v[24:27], v[144:147], v[202:205], v[24:27]
	v_mfma_f32_16x16x32_bf16 v[24:27], v[148:151], v[206:209], v[24:27]
	v_mfma_f32_16x16x32_bf16 v[20:23], v[152:155], v[202:205], v[20:23]
	v_mfma_f32_16x16x32_bf16 v[20:23], v[156:159], v[206:209], v[20:23]
	v_mfma_f32_16x16x32_bf16 v[32:35], v[164:167], v[202:205], v[32:35]
	v_mfma_f32_16x16x32_bf16 v[32:35], v[168:171], v[206:209], v[32:35]
	v_mfma_f32_16x16x32_bf16 v[28:31], v[172:175], v[202:205], v[28:31]
	v_mfma_f32_16x16x32_bf16 v[28:31], v[176:179], v[206:209], v[28:31]
	v_mfma_f32_16x16x32_bf16 v[12:15], v[172:175], v[216:219], v[12:15]
	v_mfma_f32_16x16x32_bf16 v[12:15], v[176:179], v[220:223], v[12:15]
	v_mfma_f32_16x16x32_bf16 v[16:19], v[164:167], v[216:219], v[16:19]
	v_mfma_f32_16x16x32_bf16 v[16:19], v[168:171], v[220:223], v[16:19]
	v_mfma_f32_16x16x32_bf16 v[4:7], v[152:155], v[216:219], v[4:7]
	v_mfma_f32_16x16x32_bf16 v[4:7], v[156:159], v[220:223], v[4:7]
	v_mfma_f32_16x16x32_bf16 v[8:11], v[144:147], v[216:219], v[8:11]
	v_mfma_f32_16x16x32_bf16 v[8:11], v[148:151], v[220:223], v[8:11]
	s_barrier
; #define PG8_MMA(ai, bj, At, Bt) do { __builtin_amdgcn_s_setprio(1); _Pragma("unroll") for (int m = 0; m < 4; ++m) _Pragma("unroll") for (int n = 0; n < 2; ++n) _Pragma("unroll") for (int k = 0; k < 2; ++k) \
;         acc[ai][bj][m][n] = __builtin_amdgcn_mfma_f32_16x16x32_bf16(Bt[n][k], At[m][k], acc[ai][bj][m][n], 0, 0, 0); __builtin_amdgcn_s_setprio(0); } while (0)
; #define PG8_WAIT_V(n) asm volatile("s_waitcnt vmcnt(" #n ")" ::: "memory")
; #define PG8_TRIP_HEAD(T) const int t = (T); const bool last = (t == nt - 2); \
;             const char* a1 = cA + (size_t)(t + 1) * kstep; \
;             const char* a2 = last ? nA : cA + (size_t)(t + 2) * kstep; const char* b2 = last ? nB : cB + (size_t)(t + 2) * kstep; \
;             const char* a3 = a2 + kstep; const char* b3 = b2 + kstep; \
;             if (last && has_next) S.a_ready(nxt);
; template <class Epi, class Sched, bool ALIGN_EPI = false, bool SP2 = false>
; __device__ __forceinline__ void gemm_phase(PG8_LAS unsigned char* lds, const Gemm g, const Sched& S, const Epi& E) {
;     ...
;         if constexpr (SP2) {
;             { PG8_TRIP_HEAD(0) PG8_TRIP_SP2(asm volatile("s_waitcnt vmcnt(%0)" :: "n"(8 + Epi::NST) : "memory"), PG8_MMAZ) }
;             for (int tt = 2; tt < nt; tt += 2) { PG8_TRIP_HEAD(tt) PG8_TRIP_SP2(PG8_WAIT_V(8), PG8_MMA) }
	ds_read_b128 v[144:147], v142
	ds_read_b128 v[148:151], v142 offset:1024
	ds_read_b128 v[152:155], v142 offset:2048
	ds_read_b128 v[156:159], v142 offset:3072
	ds_read_b128 v[164:167], v143
	ds_read_b128 v[168:171], v143 offset:1024
	ds_read_b128 v[172:175], v143 offset:2048
	ds_read_b128 v[176:179], v143 offset:3072
	s_mov_b32 m0, s39
	ds_read_b128 v[180:183], v163 offset:32768
	ds_read_b128 v[190:193], v163 offset:33792
	ds_read_b128 v[194:197], v163 offset:34816
	ds_read_b128 v[198:201], v163 offset:35840
	ds_read_b128 v[202:205], v163 offset:36864
	ds_read_b128 v[206:209], v163 offset:37888
	ds_read_b128 v[216:219], v163 offset:38912
	ds_read_b128 v[220:223], v163 offset:39936
	s_add_u32 s70, s54, s82
	s_addc_u32 s71, s55, s83
	global_load_lds_dwordx4 v134, s[70:71]
	s_mov_b32 m0, s40
	s_nop 0
	s_add_u32 s70, s54, s68
	s_addc_u32 s71, s55, s69
	global_load_lds_dwordx4 v134, s[70:71]
	s_waitcnt vmcnt(8)
	s_waitcnt lgkmcnt(0)
	s_barrier
	v_mfma_f32_16x16x32_bf16 v[120:123], v[144:147], v[180:183], v[120:123]
	v_mfma_f32_16x16x32_bf16 v[120:123], v[148:151], v[190:193], v[120:123]
	v_mfma_f32_16x16x32_bf16 v[116:119], v[152:155], v[180:183], v[116:119]
	v_mfma_f32_16x16x32_bf16 v[116:119], v[156:159], v[190:193], v[116:119]
	v_mfma_f32_16x16x32_bf16 v[128:131], v[164:167], v[180:183], v[128:131]
	v_mfma_f32_16x16x32_bf16 v[128:131], v[168:171], v[190:193], v[128:131]
	v_mfma_f32_16x16x32_bf16 v[124:127], v[172:175], v[180:183], v[124:127]
	v_mfma_f32_16x16x32_bf16 v[124:127], v[176:179], v[190:193], v[124:127]
	v_mfma_f32_16x16x32_bf16 v[108:111], v[172:175], v[194:197], v[108:111]
	v_mfma_f32_16x16x32_bf16 v[108:111], v[176:179], v[198:201], v[108:111]
	v_mfma_f32_16x16x32_bf16 v[112:115], v[164:167], v[194:197], v[112:115]
	v_mfma_f32_16x16x32_bf16 v[112:115], v[168:171], v[198:201], v[112:115]
	v_mfma_f32_16x16x32_bf16 v[100:103], v[152:155], v[194:197], v[100:103]
	v_mfma_f32_16x16x32_bf16 v[100:103], v[156:159], v[198:201], v[100:103]
	v_mfma_f32_16x16x32_bf16 v[104:107], v[144:147], v[194:197], v[104:107]
	v_mfma_f32_16x16x32_bf16 v[104:107], v[148:151], v[198:201], v[104:107]
	v_mfma_f32_16x16x32_bf16 v[88:91], v[144:147], v[202:205], v[88:91]
	v_mfma_f32_16x16x32_bf16 v[88:91], v[148:151], v[206:209], v[88:91]
	v_mfma_f32_16x16x32_bf16 v[84:87], v[152:155], v[202:205], v[84:87]
	v_mfma_f32_16x16x32_bf16 v[84:87], v[156:159], v[206:209], v[84:87]
	v_mfma_f32_16x16x32_bf16 v[96:99], v[164:167], v[202:205], v[96:99]
	v_mfma_f32_16x16x32_bf16 v[96:99], v[168:171], v[206:209], v[96:99]
	v_mfma_f32_16x16x32_bf16 v[92:95], v[172:175], v[202:205], v[92:95]
	v_mfma_f32_16x16x32_bf16 v[92:95], v[176:179], v[206:209], v[92:95]
	v_mfma_f32_16x16x32_bf16 v[76:79], v[172:175], v[216:219], v[76:79]
	v_mfma_f32_16x16x32_bf16 v[76:79], v[176:179], v[220:223], v[76:79]
	v_mfma_f32_16x16x32_bf16 v[80:83], v[164:167], v[216:219], v[80:83]
	v_mfma_f32_16x16x32_bf16 v[80:83], v[168:171], v[220:223], v[80:83]
	v_mfma_f32_16x16x32_bf16 v[68:71], v[152:155], v[216:219], v[68:71]
	v_mfma_f32_16x16x32_bf16 v[68:71], v[156:159], v[220:223], v[68:71]
	v_mfma_f32_16x16x32_bf16 v[72:75], v[144:147], v[216:219], v[72:75]
	v_mfma_f32_16x16x32_bf16 v[72:75], v[148:151], v[220:223], v[72:75]
	s_barrier
	s_mov_b32 m0, s49
	ds_read_b128 v[180:183], v163 offset:49152
	ds_read_b128 v[190:193], v163 offset:50176
	ds_read_b128 v[194:197], v163 offset:51200
	ds_read_b128 v[198:201], v163 offset:52224
	ds_read_b128 v[202:205], v163 offset:53248
	ds_read_b128 v[206:209], v163 offset:54272
	ds_read_b128 v[216:219], v163 offset:55296
	ds_read_b128 v[220:223], v163 offset:56320
	s_add_u32 s70, s56, s78
	s_addc_u32 s71, s57, s79
	global_load_lds_dwordx4 v132, s[70:71]
	s_mov_b32 m0, s50
	s_nop 0
	s_add_u32 s70, s56, s84
	s_addc_u32 s71, s57, s85
	global_load_lds_dwordx4 v132, s[70:71]
	s_mov_b32 m0, s51
	s_add_u32 s70, s56, s62
	s_addc_u32 s71, s57, s63
	global_load_lds_dwordx4 v132, s[70:71]
	s_mov_b32 m0, s52
	s_nop 0
	s_add_u32 s70, s56, s66
	s_addc_u32 s71, s57, s67
	global_load_lds_dwordx4 v132, s[70:71]
	s_mov_b32 m0, s0
	s_nop 0
	s_add_u32 s70, s54, s78
	s_addc_u32 s71, s55, s79
	global_load_lds_dwordx4 v134, s[70:71]
	s_mov_b32 m0, s41
	s_nop 0
	s_add_u32 s70, s54, s92
	s_addc_u32 s71, s55, s93
	global_load_lds_dwordx4 v134, s[70:71]
	s_waitcnt vmcnt(8)
	s_waitcnt lgkmcnt(0)
	s_barrier
	v_mfma_f32_16x16x32_bf16 v[56:59], v[144:147], v[180:183], v[56:59]
	v_mfma_f32_16x16x32_bf16 v[56:59], v[148:151], v[190:193], v[56:59]
	v_mfma_f32_16x16x32_bf16 v[52:55], v[152:155], v[180:183], v[52:55]
	v_mfma_f32_16x16x32_bf16 v[52:55], v[156:159], v[190:193], v[52:55]
	v_mfma_f32_16x16x32_bf16 v[64:67], v[164:167], v[180:183], v[64:67]
	v_mfma_f32_16x16x32_bf16 v[64:67], v[168:171], v[190:193], v[64:67]
	v_mfma_f32_16x16x32_bf16 v[60:63], v[172:175], v[180:183], v[60:63]
	v_mfma_f32_16x16x32_bf16 v[60:63], v[176:179], v[190:193], v[60:63]
	v_mfma_f32_16x16x32_bf16 v[44:47], v[172:175], v[194:197], v[44:47]
	v_mfma_f32_16x16x32_bf16 v[44:47], v[176:179], v[198:201], v[44:47]
	v_mfma_f32_16x16x32_bf16 v[48:51], v[164:167], v[194:197], v[48:51]
	v_mfma_f32_16x16x32_bf16 v[48:51], v[168:171], v[198:201], v[48:51]
	v_mfma_f32_16x16x32_bf16 v[36:39], v[152:155], v[194:197], v[36:39]
	v_mfma_f32_16x16x32_bf16 v[36:39], v[156:159], v[198:201], v[36:39]
	v_mfma_f32_16x16x32_bf16 v[40:43], v[144:147], v[194:197], v[40:43]
	v_mfma_f32_16x16x32_bf16 v[40:43], v[148:151], v[198:201], v[40:43]
	v_mfma_f32_16x16x32_bf16 v[24:27], v[144:147], v[202:205], v[24:27]
	v_mfma_f32_16x16x32_bf16 v[24:27], v[148:151], v[206:209], v[24:27]
	v_mfma_f32_16x16x32_bf16 v[20:23], v[152:155], v[202:205], v[20:23]
	v_mfma_f32_16x16x32_bf16 v[20:23], v[156:159], v[206:209], v[20:23]
	v_mfma_f32_16x16x32_bf16 v[32:35], v[164:167], v[202:205], v[32:35]
	v_mfma_f32_16x16x32_bf16 v[32:35], v[168:171], v[206:209], v[32:35]
	v_mfma_f32_16x16x32_bf16 v[28:31], v[172:175], v[202:205], v[28:31]
	v_mfma_f32_16x16x32_bf16 v[28:31], v[176:179], v[206:209], v[28:31]
	v_mfma_f32_16x16x32_bf16 v[12:15], v[172:175], v[216:219], v[12:15]
	v_mfma_f32_16x16x32_bf16 v[12:15], v[176:179], v[220:223], v[12:15]
	v_mfma_f32_16x16x32_bf16 v[16:19], v[164:167], v[216:219], v[16:19]
	v_mfma_f32_16x16x32_bf16 v[16:19], v[168:171], v[220:223], v[16:19]
	v_mfma_f32_16x16x32_bf16 v[4:7], v[152:155], v[216:219], v[4:7]
	v_mfma_f32_16x16x32_bf16 v[4:7], v[156:159], v[220:223], v[4:7]
	v_mfma_f32_16x16x32_bf16 v[8:11], v[144:147], v[216:219], v[8:11]
	v_mfma_f32_16x16x32_bf16 v[8:11], v[148:151], v[220:223], v[8:11]
	s_barrier
	s_add_i32 s30, s30, 2
	s_add_u32 s10, s10, 0x100
	s_addc_u32 s11, s11, 0
	s_add_u32 s28, s28, 0x100
	s_addc_u32 s29, s29, 0
	s_cmp_gt_u32 s30, 29
	s_cbranch_scc0 .LBB0_130
	s_and_b64 vcc, exec, s[20:21]
	s_cbranch_vccz .LBB0_133
	s_barrier

.LBB0_233:
	ds_read_b128 v[120:123], v116
	ds_read_b128 v[132:135], v116 offset:1024
	ds_read_b128 v[144:147], v116 offset:2048
	ds_read_b128 v[148:151], v116 offset:3072
	ds_read_b128 v[152:155], v117
	ds_read_b128 v[156:159], v117 offset:1024
	ds_read_b128 v[166:169], v117 offset:2048
	ds_read_b128 v[170:173], v117 offset:3072
	s_add_u32 s49, s26, 0xffea0080
	s_addc_u32 s50, s27, -1
	s_cmpk_eq_i32 s48, 0x54
	s_cselect_b32 s51, s21, s50
	s_cselect_b32 s50, s20, s49
	s_cselect_b32 s53, s23, s25
	s_cselect_b32 s52, s22, s24
	s_mov_b32 m0, s0
	ds_read_b128 v[180:183], v178
	ds_read_b128 v[184:187], v178 offset:1024
	ds_read_b128 v[190:193], v178 offset:2048
	ds_read_b128 v[194:197], v178 offset:3072
	ds_read_b128 v[198:201], v178 offset:4096
	ds_read_b128 v[202:205], v178 offset:5120
	ds_read_b128 v[206:209], v178 offset:6144
	ds_read_b128 v[216:219], v178 offset:7168
	global_load_lds_dwordx4 v164, s[26:27]
	s_mov_b32 m0, s4
	s_nop 0
	s_add_u32 s70, s26, s86
	s_addc_u32 s71, s27, s87
	global_load_lds_dwordx4 v164, s[70:71]
	s_waitcnt vmcnt(8)
	s_waitcnt lgkmcnt(0)
	s_barrier
	v_mfma_f32_16x16x32_bf16 v[140:143], v[120:123], v[180:183], v[140:143]
	v_mfma_f32_16x16x32_bf16 v[140:143], v[132:135], v[184:187], v[140:143]
	v_mfma_f32_16x16x32_bf16 v[136:139], v[144:147], v[180:183], v[136:139]
	v_mfma_f32_16x16x32_bf16 v[136:139], v[148:151], v[184:187], v[136:139]
	v_mfma_f32_16x16x32_bf16 v[128:131], v[152:155], v[180:183], v[128:131]
	v_mfma_f32_16x16x32_bf16 v[128:131], v[156:159], v[184:187], v[128:131]
	v_mfma_f32_16x16x32_bf16 v[124:127], v[166:169], v[180:183], v[124:127]
	v_mfma_f32_16x16x32_bf16 v[124:127], v[170:173], v[184:187], v[124:127]
	v_mfma_f32_16x16x32_bf16 v[100:103], v[166:169], v[190:193], v[100:103]
	v_mfma_f32_16x16x32_bf16 v[100:103], v[170:173], v[194:197], v[100:103]
	v_mfma_f32_16x16x32_bf16 v[104:107], v[152:155], v[190:193], v[104:107]
	v_mfma_f32_16x16x32_bf16 v[104:107], v[156:159], v[194:197], v[104:107]
	v_mfma_f32_16x16x32_bf16 v[108:111], v[144:147], v[190:193], v[108:111]
	v_mfma_f32_16x16x32_bf16 v[108:111], v[148:151], v[194:197], v[108:111]
	v_mfma_f32_16x16x32_bf16 v[112:115], v[120:123], v[190:193], v[112:115]
	v_mfma_f32_16x16x32_bf16 v[112:115], v[132:135], v[194:197], v[112:115]
	v_mfma_f32_16x16x32_bf16 v[96:99], v[120:123], v[198:201], v[96:99]
	v_mfma_f32_16x16x32_bf16 v[96:99], v[132:135], v[202:205], v[96:99]
	v_mfma_f32_16x16x32_bf16 v[92:95], v[144:147], v[198:201], v[92:95]
	v_mfma_f32_16x16x32_bf16 v[92:95], v[148:151], v[202:205], v[92:95]
	v_mfma_f32_16x16x32_bf16 v[88:91], v[152:155], v[198:201], v[88:91]
	v_mfma_f32_16x16x32_bf16 v[88:91], v[156:159], v[202:205], v[88:91]
	v_mfma_f32_16x16x32_bf16 v[84:87], v[166:169], v[198:201], v[84:87]
	v_mfma_f32_16x16x32_bf16 v[84:87], v[170:173], v[202:205], v[84:87]
	v_mfma_f32_16x16x32_bf16 v[68:71], v[166:169], v[206:209], v[68:71]
	v_mfma_f32_16x16x32_bf16 v[68:71], v[170:173], v[216:219], v[68:71]
	v_mfma_f32_16x16x32_bf16 v[72:75], v[152:155], v[206:209], v[72:75]
	v_mfma_f32_16x16x32_bf16 v[72:75], v[156:159], v[216:219], v[72:75]
	v_mfma_f32_16x16x32_bf16 v[76:79], v[144:147], v[206:209], v[76:79]
	v_mfma_f32_16x16x32_bf16 v[76:79], v[148:151], v[216:219], v[76:79]
	v_mfma_f32_16x16x32_bf16 v[80:83], v[120:123], v[206:209], v[80:83]
	v_mfma_f32_16x16x32_bf16 v[80:83], v[132:135], v[216:219], v[80:83]
	s_barrier
	s_mov_b32 m0, s5
	ds_read_b128 v[180:183], v178 offset:16384
	ds_read_b128 v[184:187], v178 offset:17408
	ds_read_b128 v[190:193], v178 offset:18432
	ds_read_b128 v[194:197], v178 offset:19456
	ds_read_b128 v[198:201], v178 offset:20480
	ds_read_b128 v[202:205], v178 offset:21504
	ds_read_b128 v[206:209], v178 offset:22528
	ds_read_b128 v[216:219], v178 offset:23552
	global_load_lds_dwordx4 v162, s[52:53]
	s_mov_b32 m0, s33
	s_nop 0
	s_add_u32 s70, s52, s86
	s_addc_u32 s71, s53, s87
	global_load_lds_dwordx4 v162, s[70:71]
	s_mov_b32 m0, s42
	s_nop 0
	s_add_u32 s70, s52, s54
	s_addc_u32 s71, s53, s55
	global_load_lds_dwordx4 v162, s[70:71]
	s_mov_b32 m0, s43
	s_nop 0
	s_add_u32 s70, s52, s56
	s_addc_u32 s71, s53, s57
	global_load_lds_dwordx4 v162, s[70:71]
	s_mov_b32 m0, s31
	s_nop 0
	global_load_lds_dwordx4 v160, s[50:51]
	s_mov_b32 m0, s34
	s_nop 0
	s_add_u32 s70, s50, s86
	s_addc_u32 s71, s51, s87
	global_load_lds_dwordx4 v160, s[70:71]
	s_waitcnt vmcnt(8)
	s_waitcnt lgkmcnt(0)
	s_barrier
	v_mfma_f32_16x16x32_bf16 v[56:59], v[120:123], v[180:183], v[56:59]
	v_mfma_f32_16x16x32_bf16 v[56:59], v[132:135], v[184:187], v[56:59]
	v_mfma_f32_16x16x32_bf16 v[52:55], v[144:147], v[180:183], v[52:55]
	v_mfma_f32_16x16x32_bf16 v[52:55], v[148:151], v[184:187], v[52:55]
	v_mfma_f32_16x16x32_bf16 v[64:67], v[152:155], v[180:183], v[64:67]
	v_mfma_f32_16x16x32_bf16 v[64:67], v[156:159], v[184:187], v[64:67]
	v_mfma_f32_16x16x32_bf16 v[60:63], v[166:169], v[180:183], v[60:63]
	v_mfma_f32_16x16x32_bf16 v[60:63], v[170:173], v[184:187], v[60:63]
	v_mfma_f32_16x16x32_bf16 v[36:39], v[166:169], v[190:193], v[36:39]
	v_mfma_f32_16x16x32_bf16 v[36:39], v[170:173], v[194:197], v[36:39]
	v_mfma_f32_16x16x32_bf16 v[40:43], v[152:155], v[190:193], v[40:43]
	v_mfma_f32_16x16x32_bf16 v[40:43], v[156:159], v[194:197], v[40:43]
	v_mfma_f32_16x16x32_bf16 v[44:47], v[144:147], v[190:193], v[44:47]
	v_mfma_f32_16x16x32_bf16 v[44:47], v[148:151], v[194:197], v[44:47]
	v_mfma_f32_16x16x32_bf16 v[48:51], v[120:123], v[190:193], v[48:51]
	v_mfma_f32_16x16x32_bf16 v[48:51], v[132:135], v[194:197], v[48:51]
	v_mfma_f32_16x16x32_bf16 v[32:35], v[120:123], v[198:201], v[32:35]
	v_mfma_f32_16x16x32_bf16 v[32:35], v[132:135], v[202:205], v[32:35]
	v_mfma_f32_16x16x32_bf16 v[28:31], v[144:147], v[198:201], v[28:31]
	v_mfma_f32_16x16x32_bf16 v[28:31], v[148:151], v[202:205], v[28:31]
	v_mfma_f32_16x16x32_bf16 v[24:27], v[152:155], v[198:201], v[24:27]
	v_mfma_f32_16x16x32_bf16 v[24:27], v[156:159], v[202:205], v[24:27]
	v_mfma_f32_16x16x32_bf16 v[20:23], v[166:169], v[198:201], v[20:23]
	v_mfma_f32_16x16x32_bf16 v[20:23], v[170:173], v[202:205], v[20:23]
	v_mfma_f32_16x16x32_bf16 v[4:7], v[166:169], v[206:209], v[4:7]
	v_mfma_f32_16x16x32_bf16 v[4:7], v[170:173], v[216:219], v[4:7]
	v_mfma_f32_16x16x32_bf16 v[8:11], v[152:155], v[206:209], v[8:11]
	v_mfma_f32_16x16x32_bf16 v[8:11], v[156:159], v[216:219], v[8:11]
	v_mfma_f32_16x16x32_bf16 v[12:15], v[144:147], v[206:209], v[12:15]
	v_mfma_f32_16x16x32_bf16 v[12:15], v[148:151], v[216:219], v[12:15]
	v_mfma_f32_16x16x32_bf16 v[16:19], v[120:123], v[206:209], v[16:19]
	v_mfma_f32_16x16x32_bf16 v[16:19], v[132:135], v[216:219], v[16:19]
	s_barrier
; #define PG8_MMA(ai, bj, At, Bt) do { __builtin_amdgcn_s_setprio(1); _Pragma("unroll") for (int m = 0; m < 4; ++m) _Pragma("unroll") for (int n = 0; n < 2; ++n) _Pragma("unroll") for (int k = 0; k < 2; ++k) \
;         acc[ai][bj][m][n] = __builtin_amdgcn_mfma_f32_16x16x32_bf16(Bt[n][k], At[m][k], acc[ai][bj][m][n], 0, 0, 0); __builtin_amdgcn_s_setprio(0); } while (0)
; #define PG8_WAIT_V(n) asm volatile("s_waitcnt vmcnt(" #n ")" ::: "memory")
; #define PG8_TRIP_HEAD(T) const int t = (T); const bool last = (t == nt - 2); \
;             const char* a1 = cA + (size_t)(t + 1) * kstep; \
;             const char* a2 = last ? nA : cA + (size_t)(t + 2) * kstep; const char* b2 = last ? nB : cB + (size_t)(t + 2) * kstep; \
;             const char* a3 = a2 + kstep; const char* b3 = b2 + kstep; \
;             if (last && has_next) S.a_ready(nxt);
; template <class Epi, class Sched, bool ALIGN_EPI = false, bool SP2 = false>
; __device__ __forceinline__ void gemm_phase(PG8_LAS unsigned char* lds, const Gemm g, const Sched& S, const Epi& E) {
;     ...
;         if constexpr (SP2) {
;             { PG8_TRIP_HEAD(0) PG8_TRIP_SP2(asm volatile("s_waitcnt vmcnt(%0)" :: "n"(8 + Epi::NST) : "memory"), PG8_MMAZ) }
;             for (int tt = 2; tt < nt; tt += 2) { PG8_TRIP_HEAD(tt) PG8_TRIP_SP2(PG8_WAIT_V(8), PG8_MMA) }
	ds_read_b128 v[120:123], v118
	ds_read_b128 v[132:135], v118 offset:1024
	ds_read_b128 v[144:147], v118 offset:2048
	ds_read_b128 v[148:151], v118 offset:3072
	ds_read_b128 v[152:155], v119
	ds_read_b128 v[156:159], v119 offset:1024
	ds_read_b128 v[166:169], v119 offset:2048
	ds_read_b128 v[170:173], v119 offset:3072
	s_mov_b32 m0, s35
	ds_read_b128 v[180:183], v178 offset:32768
	ds_read_b128 v[184:187], v178 offset:33792
	ds_read_b128 v[190:193], v178 offset:34816
	ds_read_b128 v[194:197], v178 offset:35840
	ds_read_b128 v[198:201], v178 offset:36864
	ds_read_b128 v[202:205], v178 offset:37888
	ds_read_b128 v[206:209], v178 offset:38912
	ds_read_b128 v[216:219], v178 offset:39936
	s_add_u32 s70, s50, s54
	s_addc_u32 s71, s51, s55
	global_load_lds_dwordx4 v160, s[70:71]
	s_mov_b32 m0, s36
	s_nop 0
	s_add_u32 s70, s50, s56
	s_addc_u32 s71, s51, s57
	global_load_lds_dwordx4 v160, s[70:71]
	s_waitcnt vmcnt(8)
	s_waitcnt lgkmcnt(0)
	s_barrier
	v_mfma_f32_16x16x32_bf16 v[140:143], v[120:123], v[180:183], v[140:143]
	v_mfma_f32_16x16x32_bf16 v[140:143], v[132:135], v[184:187], v[140:143]
	v_mfma_f32_16x16x32_bf16 v[136:139], v[144:147], v[180:183], v[136:139]
	v_mfma_f32_16x16x32_bf16 v[136:139], v[148:151], v[184:187], v[136:139]
	v_mfma_f32_16x16x32_bf16 v[128:131], v[152:155], v[180:183], v[128:131]
	v_mfma_f32_16x16x32_bf16 v[128:131], v[156:159], v[184:187], v[128:131]
	v_mfma_f32_16x16x32_bf16 v[124:127], v[166:169], v[180:183], v[124:127]
	v_mfma_f32_16x16x32_bf16 v[124:127], v[170:173], v[184:187], v[124:127]
	v_mfma_f32_16x16x32_bf16 v[100:103], v[166:169], v[190:193], v[100:103]
	v_mfma_f32_16x16x32_bf16 v[100:103], v[170:173], v[194:197], v[100:103]
	v_mfma_f32_16x16x32_bf16 v[104:107], v[152:155], v[190:193], v[104:107]
	v_mfma_f32_16x16x32_bf16 v[104:107], v[156:159], v[194:197], v[104:107]
	v_mfma_f32_16x16x32_bf16 v[108:111], v[144:147], v[190:193], v[108:111]
	v_mfma_f32_16x16x32_bf16 v[108:111], v[148:151], v[194:197], v[108:111]
	v_mfma_f32_16x16x32_bf16 v[112:115], v[120:123], v[190:193], v[112:115]
	v_mfma_f32_16x16x32_bf16 v[112:115], v[132:135], v[194:197], v[112:115]
	v_mfma_f32_16x16x32_bf16 v[96:99], v[120:123], v[198:201], v[96:99]
	v_mfma_f32_16x16x32_bf16 v[96:99], v[132:135], v[202:205], v[96:99]
	v_mfma_f32_16x16x32_bf16 v[92:95], v[144:147], v[198:201], v[92:95]
	v_mfma_f32_16x16x32_bf16 v[92:95], v[148:151], v[202:205], v[92:95]
	v_mfma_f32_16x16x32_bf16 v[88:91], v[152:155], v[198:201], v[88:91]
	v_mfma_f32_16x16x32_bf16 v[88:91], v[156:159], v[202:205], v[88:91]
	v_mfma_f32_16x16x32_bf16 v[84:87], v[166:169], v[198:201], v[84:87]
	v_mfma_f32_16x16x32_bf16 v[84:87], v[170:173], v[202:205], v[84:87]
	v_mfma_f32_16x16x32_bf16 v[68:71], v[166:169], v[206:209], v[68:71]
	v_mfma_f32_16x16x32_bf16 v[68:71], v[170:173], v[216:219], v[68:71]
	v_mfma_f32_16x16x32_bf16 v[72:75], v[152:155], v[206:209], v[72:75]
	v_mfma_f32_16x16x32_bf16 v[72:75], v[156:159], v[216:219], v[72:75]
	v_mfma_f32_16x16x32_bf16 v[76:79], v[144:147], v[206:209], v[76:79]
	v_mfma_f32_16x16x32_bf16 v[76:79], v[148:151], v[216:219], v[76:79]
	v_mfma_f32_16x16x32_bf16 v[80:83], v[120:123], v[206:209], v[80:83]
	v_mfma_f32_16x16x32_bf16 v[80:83], v[132:135], v[216:219], v[80:83]
	s_barrier
	s_mov_b32 m0, s44
	ds_read_b128 v[180:183], v178 offset:49152
	ds_read_b128 v[184:187], v178 offset:50176
	ds_read_b128 v[190:193], v178 offset:51200
	ds_read_b128 v[194:197], v178 offset:52224
	ds_read_b128 v[198:201], v178 offset:53248
	ds_read_b128 v[202:205], v178 offset:54272
	ds_read_b128 v[206:209], v178 offset:55296
	ds_read_b128 v[216:219], v178 offset:56320
	s_add_u32 s70, s52, s78
	s_addc_u32 s71, s53, s79
	global_load_lds_dwordx4 v162, s[70:71]
	s_mov_b32 m0, s45
	s_nop 0
	s_add_u32 s70, s52, s60
	s_addc_u32 s71, s53, s61
	global_load_lds_dwordx4 v162, s[70:71]
	s_mov_b32 m0, s46
	s_add_u32 s70, s52, s62
	s_addc_u32 s71, s53, s63
	global_load_lds_dwordx4 v162, s[70:71]
	s_mov_b32 m0, s47
	s_nop 0
	s_add_u32 s70, s52, s64
	s_addc_u32 s71, s53, s65
	global_load_lds_dwordx4 v162, s[70:71]
	s_mov_b32 m0, s37
	s_nop 0
	s_add_u32 s70, s50, s78
	s_addc_u32 s71, s51, s79
	global_load_lds_dwordx4 v160, s[70:71]
	s_mov_b32 m0, s38
	s_nop 0
	s_add_u32 s70, s50, s60
	s_addc_u32 s71, s51, s61
	global_load_lds_dwordx4 v160, s[70:71]
	s_waitcnt vmcnt(8)
	s_waitcnt lgkmcnt(0)
	s_barrier
	v_mfma_f32_16x16x32_bf16 v[56:59], v[120:123], v[180:183], v[56:59]
	v_mfma_f32_16x16x32_bf16 v[56:59], v[132:135], v[184:187], v[56:59]
	v_mfma_f32_16x16x32_bf16 v[52:55], v[144:147], v[180:183], v[52:55]
	v_mfma_f32_16x16x32_bf16 v[52:55], v[148:151], v[184:187], v[52:55]
	v_mfma_f32_16x16x32_bf16 v[64:67], v[152:155], v[180:183], v[64:67]
	v_mfma_f32_16x16x32_bf16 v[64:67], v[156:159], v[184:187], v[64:67]
	v_mfma_f32_16x16x32_bf16 v[60:63], v[166:169], v[180:183], v[60:63]
	v_mfma_f32_16x16x32_bf16 v[60:63], v[170:173], v[184:187], v[60:63]
	v_mfma_f32_16x16x32_bf16 v[36:39], v[166:169], v[190:193], v[36:39]
	v_mfma_f32_16x16x32_bf16 v[36:39], v[170:173], v[194:197], v[36:39]
	v_mfma_f32_16x16x32_bf16 v[40:43], v[152:155], v[190:193], v[40:43]
	v_mfma_f32_16x16x32_bf16 v[40:43], v[156:159], v[194:197], v[40:43]
	v_mfma_f32_16x16x32_bf16 v[44:47], v[144:147], v[190:193], v[44:47]
	v_mfma_f32_16x16x32_bf16 v[44:47], v[148:151], v[194:197], v[44:47]
	v_mfma_f32_16x16x32_bf16 v[48:51], v[120:123], v[190:193], v[48:51]
	v_mfma_f32_16x16x32_bf16 v[48:51], v[132:135], v[194:197], v[48:51]
	v_mfma_f32_16x16x32_bf16 v[32:35], v[120:123], v[198:201], v[32:35]
	v_mfma_f32_16x16x32_bf16 v[32:35], v[132:135], v[202:205], v[32:35]
	v_mfma_f32_16x16x32_bf16 v[28:31], v[144:147], v[198:201], v[28:31]
	v_mfma_f32_16x16x32_bf16 v[28:31], v[148:151], v[202:205], v[28:31]
	v_mfma_f32_16x16x32_bf16 v[24:27], v[152:155], v[198:201], v[24:27]
	v_mfma_f32_16x16x32_bf16 v[24:27], v[156:159], v[202:205], v[24:27]
	v_mfma_f32_16x16x32_bf16 v[20:23], v[166:169], v[198:201], v[20:23]
	v_mfma_f32_16x16x32_bf16 v[20:23], v[170:173], v[202:205], v[20:23]
	v_mfma_f32_16x16x32_bf16 v[4:7], v[166:169], v[206:209], v[4:7]
	v_mfma_f32_16x16x32_bf16 v[4:7], v[170:173], v[216:219], v[4:7]
	v_mfma_f32_16x16x32_bf16 v[8:11], v[152:155], v[206:209], v[8:11]
	v_mfma_f32_16x16x32_bf16 v[8:11], v[156:159], v[216:219], v[8:11]
	v_mfma_f32_16x16x32_bf16 v[12:15], v[144:147], v[206:209], v[12:15]
	v_mfma_f32_16x16x32_bf16 v[12:15], v[148:151], v[216:219], v[12:15]
	v_mfma_f32_16x16x32_bf16 v[16:19], v[120:123], v[206:209], v[16:19]
	v_mfma_f32_16x16x32_bf16 v[16:19], v[132:135], v[216:219], v[16:19]
	s_barrier
	s_add_i32 s48, s48, 2
	s_add_u32 s26, s26, 0x100
	s_addc_u32 s27, s27, 0
	s_add_u32 s24, s24, 0x100
	s_addc_u32 s25, s25, 0
	s_cmpk_gt_u32 s48, 0x55
	s_cbranch_scc0 .LBB0_233
	s_and_b64 vcc, exec, s[18:19]
	s_cbranch_vccz .LBB0_236
	s_barrier

.LBB0_324:
	ds_read_b128 v[136:139], v132
	ds_read_b128 v[140:143], v132 offset:1024
	ds_read_b128 v[144:147], v132 offset:2048
	ds_read_b128 v[148:151], v132 offset:3072
	ds_read_b128 v[152:155], v133
	ds_read_b128 v[156:159], v133 offset:1024
	ds_read_b128 v[160:163], v133 offset:2048
	ds_read_b128 v[174:177], v133 offset:3072
	s_add_u32 s15, s10, 0xfff7c080
	s_addc_u32 s50, s11, -1
	s_cmp_eq_u32 s14, 28
	s_cselect_b32 s51, s25, s50
	s_cselect_b32 s50, s24, s15
	s_cselect_b32 s53, s3, s13
	s_cselect_b32 s52, s4, s12
	s_mov_b32 m0, s5
	ds_read_b128 v[178:181], v200
	ds_read_b128 v[182:185], v200 offset:1024
	ds_read_b128 v[186:189], v200 offset:2048
	ds_read_b128 v[190:193], v200 offset:3072
	ds_read_b128 v[202:205], v200 offset:4096
	ds_read_b128 v[206:209], v200 offset:5120
	ds_read_b128 v[216:219], v200 offset:6144
	ds_read_b128 v[220:223], v200 offset:7168
	global_load_lds_dwordx4 v172, s[10:11]
	s_mov_b32 m0, s23
	s_nop 0
	s_add_u32 s70, s10, s96
	s_addc_u32 s71, s11, s97
	global_load_lds_dwordx4 v172, s[70:71]
	s_waitcnt vmcnt(8)
	s_waitcnt lgkmcnt(0)
	s_barrier
	v_mfma_f32_16x16x32_bf16 v[120:123], v[136:139], v[178:181], v[120:123]
	v_mfma_f32_16x16x32_bf16 v[120:123], v[140:143], v[182:185], v[120:123]
	v_mfma_f32_16x16x32_bf16 v[116:119], v[144:147], v[178:181], v[116:119]
	v_mfma_f32_16x16x32_bf16 v[116:119], v[148:151], v[182:185], v[116:119]
	v_mfma_f32_16x16x32_bf16 v[128:131], v[152:155], v[178:181], v[128:131]
	v_mfma_f32_16x16x32_bf16 v[128:131], v[156:159], v[182:185], v[128:131]
	v_mfma_f32_16x16x32_bf16 v[124:127], v[160:163], v[178:181], v[124:127]
	v_mfma_f32_16x16x32_bf16 v[124:127], v[174:177], v[182:185], v[124:127]
	v_mfma_f32_16x16x32_bf16 v[108:111], v[160:163], v[186:189], v[108:111]
	v_mfma_f32_16x16x32_bf16 v[108:111], v[174:177], v[190:193], v[108:111]
	v_mfma_f32_16x16x32_bf16 v[112:115], v[152:155], v[186:189], v[112:115]
	v_mfma_f32_16x16x32_bf16 v[112:115], v[156:159], v[190:193], v[112:115]
	v_mfma_f32_16x16x32_bf16 v[100:103], v[144:147], v[186:189], v[100:103]
	v_mfma_f32_16x16x32_bf16 v[100:103], v[148:151], v[190:193], v[100:103]
	v_mfma_f32_16x16x32_bf16 v[104:107], v[136:139], v[186:189], v[104:107]
	v_mfma_f32_16x16x32_bf16 v[104:107], v[140:143], v[190:193], v[104:107]
	v_mfma_f32_16x16x32_bf16 v[88:91], v[136:139], v[202:205], v[88:91]
	v_mfma_f32_16x16x32_bf16 v[88:91], v[140:143], v[206:209], v[88:91]
	v_mfma_f32_16x16x32_bf16 v[84:87], v[144:147], v[202:205], v[84:87]
	v_mfma_f32_16x16x32_bf16 v[84:87], v[148:151], v[206:209], v[84:87]
	v_mfma_f32_16x16x32_bf16 v[96:99], v[152:155], v[202:205], v[96:99]
	v_mfma_f32_16x16x32_bf16 v[96:99], v[156:159], v[206:209], v[96:99]
	v_mfma_f32_16x16x32_bf16 v[92:95], v[160:163], v[202:205], v[92:95]
	v_mfma_f32_16x16x32_bf16 v[92:95], v[174:177], v[206:209], v[92:95]
	v_mfma_f32_16x16x32_bf16 v[76:79], v[160:163], v[216:219], v[76:79]
	v_mfma_f32_16x16x32_bf16 v[76:79], v[174:177], v[220:223], v[76:79]
	v_mfma_f32_16x16x32_bf16 v[80:83], v[152:155], v[216:219], v[80:83]
	v_mfma_f32_16x16x32_bf16 v[80:83], v[156:159], v[220:223], v[80:83]
	v_mfma_f32_16x16x32_bf16 v[68:71], v[144:147], v[216:219], v[68:71]
	v_mfma_f32_16x16x32_bf16 v[68:71], v[148:151], v[220:223], v[68:71]
	v_mfma_f32_16x16x32_bf16 v[72:75], v[136:139], v[216:219], v[72:75]
	v_mfma_f32_16x16x32_bf16 v[72:75], v[140:143], v[220:223], v[72:75]
	s_barrier
	s_mov_b32 m0, s28
	ds_read_b128 v[178:181], v200 offset:16384
	ds_read_b128 v[182:185], v200 offset:17408
	ds_read_b128 v[186:189], v200 offset:18432
	ds_read_b128 v[190:193], v200 offset:19456
	ds_read_b128 v[202:205], v200 offset:20480
	ds_read_b128 v[206:209], v200 offset:21504
	ds_read_b128 v[216:219], v200 offset:22528
	ds_read_b128 v[220:223], v200 offset:23552
	global_load_lds_dwordx4 v164, s[52:53]
	s_mov_b32 m0, s29
	s_nop 0
	s_add_u32 s70, s52, s90
	s_addc_u32 s71, s53, s91
	global_load_lds_dwordx4 v164, s[70:71]
	s_mov_b32 m0, s33
	s_nop 0
	s_add_u32 s70, s52, s54
	s_addc_u32 s71, s53, s55
	global_load_lds_dwordx4 v164, s[70:71]
	s_mov_b32 m0, s45
	s_nop 0
	s_add_u32 s70, s52, s60
	s_addc_u32 s71, s53, s61
	global_load_lds_dwordx4 v164, s[70:71]
	s_mov_b32 m0, s30
	s_nop 0
	global_load_lds_dwordx4 v166, s[50:51]
	s_mov_b32 m0, s31
	s_nop 0
	s_add_u32 s70, s50, s96
	s_addc_u32 s71, s51, s97
	global_load_lds_dwordx4 v166, s[70:71]
	s_waitcnt vmcnt(8)
	s_waitcnt lgkmcnt(0)
	s_barrier
	v_mfma_f32_16x16x32_bf16 v[56:59], v[136:139], v[178:181], v[56:59]
	v_mfma_f32_16x16x32_bf16 v[56:59], v[140:143], v[182:185], v[56:59]
	v_mfma_f32_16x16x32_bf16 v[52:55], v[144:147], v[178:181], v[52:55]
	v_mfma_f32_16x16x32_bf16 v[52:55], v[148:151], v[182:185], v[52:55]
	v_mfma_f32_16x16x32_bf16 v[64:67], v[152:155], v[178:181], v[64:67]
	v_mfma_f32_16x16x32_bf16 v[64:67], v[156:159], v[182:185], v[64:67]
	v_mfma_f32_16x16x32_bf16 v[60:63], v[160:163], v[178:181], v[60:63]
	v_mfma_f32_16x16x32_bf16 v[60:63], v[174:177], v[182:185], v[60:63]
	v_mfma_f32_16x16x32_bf16 v[44:47], v[160:163], v[186:189], v[44:47]
	v_mfma_f32_16x16x32_bf16 v[44:47], v[174:177], v[190:193], v[44:47]
	v_mfma_f32_16x16x32_bf16 v[48:51], v[152:155], v[186:189], v[48:51]
	v_mfma_f32_16x16x32_bf16 v[48:51], v[156:159], v[190:193], v[48:51]
	v_mfma_f32_16x16x32_bf16 v[36:39], v[144:147], v[186:189], v[36:39]
	v_mfma_f32_16x16x32_bf16 v[36:39], v[148:151], v[190:193], v[36:39]
	v_mfma_f32_16x16x32_bf16 v[40:43], v[136:139], v[186:189], v[40:43]
	v_mfma_f32_16x16x32_bf16 v[40:43], v[140:143], v[190:193], v[40:43]
	v_mfma_f32_16x16x32_bf16 v[24:27], v[136:139], v[202:205], v[24:27]
	v_mfma_f32_16x16x32_bf16 v[24:27], v[140:143], v[206:209], v[24:27]
	v_mfma_f32_16x16x32_bf16 v[20:23], v[144:147], v[202:205], v[20:23]
	v_mfma_f32_16x16x32_bf16 v[20:23], v[148:151], v[206:209], v[20:23]
	v_mfma_f32_16x16x32_bf16 v[32:35], v[152:155], v[202:205], v[32:35]
	v_mfma_f32_16x16x32_bf16 v[32:35], v[156:159], v[206:209], v[32:35]
	v_mfma_f32_16x16x32_bf16 v[28:31], v[160:163], v[202:205], v[28:31]
	v_mfma_f32_16x16x32_bf16 v[28:31], v[174:177], v[206:209], v[28:31]
	v_mfma_f32_16x16x32_bf16 v[12:15], v[160:163], v[216:219], v[12:15]
	v_mfma_f32_16x16x32_bf16 v[12:15], v[174:177], v[220:223], v[12:15]
	v_mfma_f32_16x16x32_bf16 v[16:19], v[152:155], v[216:219], v[16:19]
	v_mfma_f32_16x16x32_bf16 v[16:19], v[156:159], v[220:223], v[16:19]
	v_mfma_f32_16x16x32_bf16 v[4:7], v[144:147], v[216:219], v[4:7]
	v_mfma_f32_16x16x32_bf16 v[4:7], v[148:151], v[220:223], v[4:7]
	v_mfma_f32_16x16x32_bf16 v[8:11], v[136:139], v[216:219], v[8:11]
	v_mfma_f32_16x16x32_bf16 v[8:11], v[140:143], v[220:223], v[8:11]
	s_barrier
; #define PG8_MMA(ai, bj, At, Bt) do { __builtin_amdgcn_s_setprio(1); _Pragma("unroll") for (int m = 0; m < 4; ++m) _Pragma("unroll") for (int n = 0; n < 2; ++n) _Pragma("unroll") for (int k = 0; k < 2; ++k) \
;         acc[ai][bj][m][n] = __builtin_amdgcn_mfma_f32_16x16x32_bf16(Bt[n][k], At[m][k], acc[ai][bj][m][n], 0, 0, 0); __builtin_amdgcn_s_setprio(0); } while (0)
; #define PG8_WAIT_V(n) asm volatile("s_waitcnt vmcnt(" #n ")" ::: "memory")
; #define PG8_TRIP_HEAD(T) const int t = (T); const bool last = (t == nt - 2); \
;             const char* a1 = cA + (size_t)(t + 1) * kstep; \
;             const char* a2 = last ? nA : cA + (size_t)(t + 2) * kstep; const char* b2 = last ? nB : cB + (size_t)(t + 2) * kstep; \
;             const char* a3 = a2 + kstep; const char* b3 = b2 + kstep; \
;             if (last && has_next) S.a_ready(nxt);
; template <class Epi, class Sched, bool ALIGN_EPI = false, bool SP2 = false>
; __device__ __forceinline__ void gemm_phase(PG8_LAS unsigned char* lds, const Gemm g, const Sched& S, const Epi& E) {
;     ...
;         if constexpr (SP2) {
;             { PG8_TRIP_HEAD(0) PG8_TRIP_SP2(asm volatile("s_waitcnt vmcnt(%0)" :: "n"(8 + Epi::NST) : "memory"), PG8_MMAZ) }
;             for (int tt = 2; tt < nt; tt += 2) { PG8_TRIP_HEAD(tt) PG8_TRIP_SP2(PG8_WAIT_V(8), PG8_MMA) }
	ds_read_b128 v[136:139], v134
	ds_read_b128 v[140:143], v134 offset:1024
	ds_read_b128 v[144:147], v134 offset:2048
	ds_read_b128 v[148:151], v134 offset:3072
	ds_read_b128 v[152:155], v135
	ds_read_b128 v[156:159], v135 offset:1024
	ds_read_b128 v[160:163], v135 offset:2048
	ds_read_b128 v[174:177], v135 offset:3072
	s_mov_b32 m0, s34
	ds_read_b128 v[178:181], v200 offset:32768
	ds_read_b128 v[182:185], v200 offset:33792
	ds_read_b128 v[186:189], v200 offset:34816
	ds_read_b128 v[190:193], v200 offset:35840
	ds_read_b128 v[202:205], v200 offset:36864
	ds_read_b128 v[206:209], v200 offset:37888
	ds_read_b128 v[216:219], v200 offset:38912
	ds_read_b128 v[220:223], v200 offset:39936
	s_add_u32 s70, s50, s82
	s_addc_u32 s71, s51, s83
	global_load_lds_dwordx4 v166, s[70:71]
	s_mov_b32 m0, s35
	s_nop 0
	s_add_u32 s70, s50, s64
	s_addc_u32 s71, s51, s65
	global_load_lds_dwordx4 v166, s[70:71]
	s_waitcnt vmcnt(8)
	s_waitcnt lgkmcnt(0)
	s_barrier
	v_mfma_f32_16x16x32_bf16 v[120:123], v[136:139], v[178:181], v[120:123]
	v_mfma_f32_16x16x32_bf16 v[120:123], v[140:143], v[182:185], v[120:123]
	v_mfma_f32_16x16x32_bf16 v[116:119], v[144:147], v[178:181], v[116:119]
	v_mfma_f32_16x16x32_bf16 v[116:119], v[148:151], v[182:185], v[116:119]
	v_mfma_f32_16x16x32_bf16 v[128:131], v[152:155], v[178:181], v[128:131]
	v_mfma_f32_16x16x32_bf16 v[128:131], v[156:159], v[182:185], v[128:131]
	v_mfma_f32_16x16x32_bf16 v[124:127], v[160:163], v[178:181], v[124:127]
	v_mfma_f32_16x16x32_bf16 v[124:127], v[174:177], v[182:185], v[124:127]
	v_mfma_f32_16x16x32_bf16 v[108:111], v[160:163], v[186:189], v[108:111]
	v_mfma_f32_16x16x32_bf16 v[108:111], v[174:177], v[190:193], v[108:111]
	v_mfma_f32_16x16x32_bf16 v[112:115], v[152:155], v[186:189], v[112:115]
	v_mfma_f32_16x16x32_bf16 v[112:115], v[156:159], v[190:193], v[112:115]
	v_mfma_f32_16x16x32_bf16 v[100:103], v[144:147], v[186:189], v[100:103]
	v_mfma_f32_16x16x32_bf16 v[100:103], v[148:151], v[190:193], v[100:103]
	v_mfma_f32_16x16x32_bf16 v[104:107], v[136:139], v[186:189], v[104:107]
	v_mfma_f32_16x16x32_bf16 v[104:107], v[140:143], v[190:193], v[104:107]
	v_mfma_f32_16x16x32_bf16 v[88:91], v[136:139], v[202:205], v[88:91]
	v_mfma_f32_16x16x32_bf16 v[88:91], v[140:143], v[206:209], v[88:91]
	v_mfma_f32_16x16x32_bf16 v[84:87], v[144:147], v[202:205], v[84:87]
	v_mfma_f32_16x16x32_bf16 v[84:87], v[148:151], v[206:209], v[84:87]
	v_mfma_f32_16x16x32_bf16 v[96:99], v[152:155], v[202:205], v[96:99]
	v_mfma_f32_16x16x32_bf16 v[96:99], v[156:159], v[206:209], v[96:99]
	v_mfma_f32_16x16x32_bf16 v[92:95], v[160:163], v[202:205], v[92:95]
	v_mfma_f32_16x16x32_bf16 v[92:95], v[174:177], v[206:209], v[92:95]
	v_mfma_f32_16x16x32_bf16 v[76:79], v[160:163], v[216:219], v[76:79]
	v_mfma_f32_16x16x32_bf16 v[76:79], v[174:177], v[220:223], v[76:79]
	v_mfma_f32_16x16x32_bf16 v[80:83], v[152:155], v[216:219], v[80:83]
	v_mfma_f32_16x16x32_bf16 v[80:83], v[156:159], v[220:223], v[80:83]
	v_mfma_f32_16x16x32_bf16 v[68:71], v[144:147], v[216:219], v[68:71]
	v_mfma_f32_16x16x32_bf16 v[68:71], v[148:151], v[220:223], v[68:71]
	v_mfma_f32_16x16x32_bf16 v[72:75], v[136:139], v[216:219], v[72:75]
	v_mfma_f32_16x16x32_bf16 v[72:75], v[140:143], v[220:223], v[72:75]
	s_barrier
	s_mov_b32 m0, s46
	ds_read_b128 v[178:181], v200 offset:49152
	ds_read_b128 v[182:185], v200 offset:50176
	ds_read_b128 v[186:189], v200 offset:51200
	ds_read_b128 v[190:193], v200 offset:52224
	ds_read_b128 v[202:205], v200 offset:53248
	ds_read_b128 v[206:209], v200 offset:54272
	ds_read_b128 v[216:219], v200 offset:55296
	ds_read_b128 v[220:223], v200 offset:56320
	s_add_u32 s70, s52, s78
	s_addc_u32 s71, s53, s79
	global_load_lds_dwordx4 v164, s[70:71]
	s_mov_b32 m0, s47
	s_nop 0
	s_add_u32 s70, s52, s84
	s_addc_u32 s71, s53, s85
	global_load_lds_dwordx4 v164, s[70:71]
	s_mov_b32 m0, s48
	s_add_u32 s70, s52, s56
	s_addc_u32 s71, s53, s57
	global_load_lds_dwordx4 v164, s[70:71]
	s_mov_b32 m0, s49
	s_nop 0
	s_add_u32 s70, s52, s62
	s_addc_u32 s71, s53, s63
	global_load_lds_dwordx4 v164, s[70:71]
	s_mov_b32 m0, s38
	s_nop 0
	s_add_u32 s70, s50, s78
	s_addc_u32 s71, s51, s79
	global_load_lds_dwordx4 v166, s[70:71]
	s_mov_b32 m0, s39
	s_nop 0
	s_add_u32 s70, s50, s92
	s_addc_u32 s71, s51, s93
	global_load_lds_dwordx4 v166, s[70:71]
	s_waitcnt vmcnt(8)
	s_waitcnt lgkmcnt(0)
	s_barrier
	v_mfma_f32_16x16x32_bf16 v[56:59], v[136:139], v[178:181], v[56:59]
	v_mfma_f32_16x16x32_bf16 v[56:59], v[140:143], v[182:185], v[56:59]
	v_mfma_f32_16x16x32_bf16 v[52:55], v[144:147], v[178:181], v[52:55]
	v_mfma_f32_16x16x32_bf16 v[52:55], v[148:151], v[182:185], v[52:55]
	v_mfma_f32_16x16x32_bf16 v[64:67], v[152:155], v[178:181], v[64:67]
	v_mfma_f32_16x16x32_bf16 v[64:67], v[156:159], v[182:185], v[64:67]
	v_mfma_f32_16x16x32_bf16 v[60:63], v[160:163], v[178:181], v[60:63]
	v_mfma_f32_16x16x32_bf16 v[60:63], v[174:177], v[182:185], v[60:63]
	v_mfma_f32_16x16x32_bf16 v[44:47], v[160:163], v[186:189], v[44:47]
	v_mfma_f32_16x16x32_bf16 v[44:47], v[174:177], v[190:193], v[44:47]
	v_mfma_f32_16x16x32_bf16 v[48:51], v[152:155], v[186:189], v[48:51]
	v_mfma_f32_16x16x32_bf16 v[48:51], v[156:159], v[190:193], v[48:51]
	v_mfma_f32_16x16x32_bf16 v[36:39], v[144:147], v[186:189], v[36:39]
	v_mfma_f32_16x16x32_bf16 v[36:39], v[148:151], v[190:193], v[36:39]
	v_mfma_f32_16x16x32_bf16 v[40:43], v[136:139], v[186:189], v[40:43]
	v_mfma_f32_16x16x32_bf16 v[40:43], v[140:143], v[190:193], v[40:43]
	v_mfma_f32_16x16x32_bf16 v[24:27], v[136:139], v[202:205], v[24:27]
	v_mfma_f32_16x16x32_bf16 v[24:27], v[140:143], v[206:209], v[24:27]
	v_mfma_f32_16x16x32_bf16 v[20:23], v[144:147], v[202:205], v[20:23]
	v_mfma_f32_16x16x32_bf16 v[20:23], v[148:151], v[206:209], v[20:23]
	v_mfma_f32_16x16x32_bf16 v[32:35], v[152:155], v[202:205], v[32:35]
	v_mfma_f32_16x16x32_bf16 v[32:35], v[156:159], v[206:209], v[32:35]
	v_mfma_f32_16x16x32_bf16 v[28:31], v[160:163], v[202:205], v[28:31]
	v_mfma_f32_16x16x32_bf16 v[28:31], v[174:177], v[206:209], v[28:31]
	v_mfma_f32_16x16x32_bf16 v[12:15], v[160:163], v[216:219], v[12:15]
	v_mfma_f32_16x16x32_bf16 v[12:15], v[174:177], v[220:223], v[12:15]
	v_mfma_f32_16x16x32_bf16 v[16:19], v[152:155], v[216:219], v[16:19]
	v_mfma_f32_16x16x32_bf16 v[16:19], v[156:159], v[220:223], v[16:19]
	v_mfma_f32_16x16x32_bf16 v[4:7], v[144:147], v[216:219], v[4:7]
	v_mfma_f32_16x16x32_bf16 v[4:7], v[148:151], v[220:223], v[4:7]
	v_mfma_f32_16x16x32_bf16 v[8:11], v[136:139], v[216:219], v[8:11]
	v_mfma_f32_16x16x32_bf16 v[8:11], v[140:143], v[220:223], v[8:11]
	s_barrier
	s_add_i32 s14, s14, 2
	s_add_u32 s10, s10, 0x100
	s_addc_u32 s11, s11, 0
	s_add_u32 s12, s12, 0x100
	s_addc_u32 s13, s13, 0
	s_cmp_gt_u32 s14, 29
	s_cbranch_scc0 .LBB0_324
	s_and_b64 vcc, exec, s[18:19]
	s_cbranch_vccz .LBB0_327
	s_barrier

.LBB0_594:
	ds_read_b128 v[136:139], v116
	ds_read_b128 v[140:143], v116 offset:1024
	ds_read_b128 v[144:147], v116 offset:2048
	ds_read_b128 v[148:151], v116 offset:3072
	ds_read_b128 v[152:155], v117
	ds_read_b128 v[156:159], v117 offset:1024
	ds_read_b128 v[160:163], v117 offset:2048
	ds_read_b128 v[164:167], v117 offset:3072
	s_add_u32 s43, s20, 0xfff7c080
	s_addc_u32 s44, s21, -1
	s_cmp_eq_u32 s15, 28
	s_cselect_b32 s45, s17, s44
	s_cselect_b32 s44, s16, s43
	s_cselect_b32 s47, s4, s9
	s_cselect_b32 s46, s5, s8
	s_mov_b32 m0, s33
	ds_read_b128 v[168:171], v221
	ds_read_b128 v[172:175], v221 offset:1024
	ds_read_b128 v[176:179], v221 offset:2048
	ds_read_b128 v[180:183], v221 offset:3072
	ds_read_b128 v[184:187], v221 offset:4096
	ds_read_b128 v[188:191], v221 offset:5120
	ds_read_b128 v[202:205], v221 offset:6144
	ds_read_b128 v[206:209], v221 offset:7168
	global_load_lds_dwordx4 v200, s[20:21]
	s_mov_b32 m0, s34
	s_nop 0
	s_add_u32 s70, s20, s96
	s_addc_u32 s71, s21, s97
	global_load_lds_dwordx4 v200, s[70:71]
	s_waitcnt vmcnt(8)
	s_waitcnt lgkmcnt(0)
	s_barrier
	v_mfma_f32_16x16x32_bf16 v[130:133], v[136:139], v[168:171], v[130:133]
	v_mfma_f32_16x16x32_bf16 v[130:133], v[140:143], v[172:175], v[130:133]
	v_mfma_f32_16x16x32_bf16 v[126:129], v[144:147], v[168:171], v[126:129]
	v_mfma_f32_16x16x32_bf16 v[126:129], v[148:151], v[172:175], v[126:129]
	v_mfma_f32_16x16x32_bf16 v[122:125], v[152:155], v[168:171], v[122:125]
	v_mfma_f32_16x16x32_bf16 v[122:125], v[156:159], v[172:175], v[122:125]
	v_mfma_f32_16x16x32_bf16 v[118:121], v[160:163], v[168:171], v[118:121]
	v_mfma_f32_16x16x32_bf16 v[118:121], v[164:167], v[172:175], v[118:121]
	v_mfma_f32_16x16x32_bf16 v[100:103], v[160:163], v[176:179], v[100:103]
	v_mfma_f32_16x16x32_bf16 v[100:103], v[164:167], v[180:183], v[100:103]
	v_mfma_f32_16x16x32_bf16 v[104:107], v[152:155], v[176:179], v[104:107]
	v_mfma_f32_16x16x32_bf16 v[104:107], v[156:159], v[180:183], v[104:107]
	v_mfma_f32_16x16x32_bf16 v[108:111], v[144:147], v[176:179], v[108:111]
	v_mfma_f32_16x16x32_bf16 v[108:111], v[148:151], v[180:183], v[108:111]
	v_mfma_f32_16x16x32_bf16 v[112:115], v[136:139], v[176:179], v[112:115]
	v_mfma_f32_16x16x32_bf16 v[112:115], v[140:143], v[180:183], v[112:115]
	v_mfma_f32_16x16x32_bf16 v[96:99], v[136:139], v[184:187], v[96:99]
	v_mfma_f32_16x16x32_bf16 v[96:99], v[140:143], v[188:191], v[96:99]
	v_mfma_f32_16x16x32_bf16 v[92:95], v[144:147], v[184:187], v[92:95]
	v_mfma_f32_16x16x32_bf16 v[92:95], v[148:151], v[188:191], v[92:95]
	v_mfma_f32_16x16x32_bf16 v[88:91], v[152:155], v[184:187], v[88:91]
	v_mfma_f32_16x16x32_bf16 v[88:91], v[156:159], v[188:191], v[88:91]
	v_mfma_f32_16x16x32_bf16 v[84:87], v[160:163], v[184:187], v[84:87]
	v_mfma_f32_16x16x32_bf16 v[84:87], v[164:167], v[188:191], v[84:87]
	v_mfma_f32_16x16x32_bf16 v[68:71], v[160:163], v[202:205], v[68:71]
	v_mfma_f32_16x16x32_bf16 v[68:71], v[164:167], v[206:209], v[68:71]
	v_mfma_f32_16x16x32_bf16 v[72:75], v[152:155], v[202:205], v[72:75]
	v_mfma_f32_16x16x32_bf16 v[72:75], v[156:159], v[206:209], v[72:75]
	v_mfma_f32_16x16x32_bf16 v[76:79], v[144:147], v[202:205], v[76:79]
	v_mfma_f32_16x16x32_bf16 v[76:79], v[148:151], v[206:209], v[76:79]
	v_mfma_f32_16x16x32_bf16 v[80:83], v[136:139], v[202:205], v[80:83]
	v_mfma_f32_16x16x32_bf16 v[80:83], v[140:143], v[206:209], v[80:83]
	s_barrier
	s_mov_b32 m0, s35
	ds_read_b128 v[168:171], v221 offset:16384
	ds_read_b128 v[172:175], v221 offset:17408
	ds_read_b128 v[176:179], v221 offset:18432
	ds_read_b128 v[180:183], v221 offset:19456
	ds_read_b128 v[184:187], v221 offset:20480
	ds_read_b128 v[188:191], v221 offset:21504
	ds_read_b128 v[202:205], v221 offset:22528
	ds_read_b128 v[206:209], v221 offset:23552
	global_load_lds_dwordx4 v194, s[46:47]
	s_mov_b32 m0, s36
	s_nop 0
	s_add_u32 s70, s46, s90
	s_addc_u32 s71, s47, s91
	global_load_lds_dwordx4 v194, s[70:71]
	s_mov_b32 m0, s37
	s_nop 0
	s_add_u32 s70, s46, s48
	s_addc_u32 s71, s47, s49
	global_load_lds_dwordx4 v194, s[70:71]
	s_mov_b32 m0, s38
	s_nop 0
	s_add_u32 s70, s46, s52
	s_addc_u32 s71, s47, s53
	global_load_lds_dwordx4 v194, s[70:71]
	s_mov_b32 m0, s23
	s_nop 0
	global_load_lds_dwordx4 v196, s[44:45]
	s_mov_b32 m0, s24
	s_nop 0
	s_add_u32 s70, s44, s96
	s_addc_u32 s71, s45, s97
	global_load_lds_dwordx4 v196, s[70:71]
	s_waitcnt vmcnt(8)
	s_waitcnt lgkmcnt(0)
	s_barrier
	v_mfma_f32_16x16x32_bf16 v[64:67], v[136:139], v[168:171], v[64:67]
	v_mfma_f32_16x16x32_bf16 v[64:67], v[140:143], v[172:175], v[64:67]
	v_mfma_f32_16x16x32_bf16 v[60:63], v[144:147], v[168:171], v[60:63]
	v_mfma_f32_16x16x32_bf16 v[60:63], v[148:151], v[172:175], v[60:63]
	v_mfma_f32_16x16x32_bf16 v[56:59], v[152:155], v[168:171], v[56:59]
	v_mfma_f32_16x16x32_bf16 v[56:59], v[156:159], v[172:175], v[56:59]
	v_mfma_f32_16x16x32_bf16 v[52:55], v[160:163], v[168:171], v[52:55]
	v_mfma_f32_16x16x32_bf16 v[52:55], v[164:167], v[172:175], v[52:55]
	v_mfma_f32_16x16x32_bf16 v[36:39], v[160:163], v[176:179], v[36:39]
	v_mfma_f32_16x16x32_bf16 v[36:39], v[164:167], v[180:183], v[36:39]
	v_mfma_f32_16x16x32_bf16 v[40:43], v[152:155], v[176:179], v[40:43]
	v_mfma_f32_16x16x32_bf16 v[40:43], v[156:159], v[180:183], v[40:43]
	v_mfma_f32_16x16x32_bf16 v[44:47], v[144:147], v[176:179], v[44:47]
	v_mfma_f32_16x16x32_bf16 v[44:47], v[148:151], v[180:183], v[44:47]
	v_mfma_f32_16x16x32_bf16 v[48:51], v[136:139], v[176:179], v[48:51]
	v_mfma_f32_16x16x32_bf16 v[48:51], v[140:143], v[180:183], v[48:51]
	v_mfma_f32_16x16x32_bf16 v[32:35], v[136:139], v[184:187], v[32:35]
	v_mfma_f32_16x16x32_bf16 v[32:35], v[140:143], v[188:191], v[32:35]
	v_mfma_f32_16x16x32_bf16 v[28:31], v[144:147], v[184:187], v[28:31]
	v_mfma_f32_16x16x32_bf16 v[28:31], v[148:151], v[188:191], v[28:31]
	v_mfma_f32_16x16x32_bf16 v[24:27], v[152:155], v[184:187], v[24:27]
	v_mfma_f32_16x16x32_bf16 v[24:27], v[156:159], v[188:191], v[24:27]
	v_mfma_f32_16x16x32_bf16 v[20:23], v[160:163], v[184:187], v[20:23]
	v_mfma_f32_16x16x32_bf16 v[20:23], v[164:167], v[188:191], v[20:23]
	v_mfma_f32_16x16x32_bf16 v[4:7], v[160:163], v[202:205], v[4:7]
	v_mfma_f32_16x16x32_bf16 v[4:7], v[164:167], v[206:209], v[4:7]
	v_mfma_f32_16x16x32_bf16 v[8:11], v[152:155], v[202:205], v[8:11]
	v_mfma_f32_16x16x32_bf16 v[8:11], v[156:159], v[206:209], v[8:11]
	v_mfma_f32_16x16x32_bf16 v[12:15], v[144:147], v[202:205], v[12:15]
	v_mfma_f32_16x16x32_bf16 v[12:15], v[148:151], v[206:209], v[12:15]
	v_mfma_f32_16x16x32_bf16 v[16:19], v[136:139], v[202:205], v[16:19]
	v_mfma_f32_16x16x32_bf16 v[16:19], v[140:143], v[206:209], v[16:19]
	s_barrier
; #define PG8_MMA(ai, bj, At, Bt) do { __builtin_amdgcn_s_setprio(1); _Pragma("unroll") for (int m = 0; m < 4; ++m) _Pragma("unroll") for (int n = 0; n < 2; ++n) _Pragma("unroll") for (int k = 0; k < 2; ++k) \
;         acc[ai][bj][m][n] = __builtin_amdgcn_mfma_f32_16x16x32_bf16(Bt[n][k], At[m][k], acc[ai][bj][m][n], 0, 0, 0); __builtin_amdgcn_s_setprio(0); } while (0)
; #define PG8_WAIT_V(n) asm volatile("s_waitcnt vmcnt(" #n ")" ::: "memory")
; #define PG8_TRIP_HEAD(T) const int t = (T); const bool last = (t == nt - 2); \
;             const char* a1 = cA + (size_t)(t + 1) * kstep; \
;             const char* a2 = last ? nA : cA + (size_t)(t + 2) * kstep; const char* b2 = last ? nB : cB + (size_t)(t + 2) * kstep; \
;             const char* a3 = a2 + kstep; const char* b3 = b2 + kstep; \
;             if (last && has_next) S.a_ready(nxt);
; template <class Epi, class Sched, bool ALIGN_EPI = false, bool SP2 = false>
; __device__ __forceinline__ void gemm_phase(PG8_LAS unsigned char* lds, const Gemm g, const Sched& S, const Epi& E) {
;     ...
;         if constexpr (SP2) {
;             { PG8_TRIP_HEAD(0) PG8_TRIP_SP2(asm volatile("s_waitcnt vmcnt(%0)" :: "n"(8 + Epi::NST) : "memory"), PG8_MMAZ) }
;             for (int tt = 2; tt < nt; tt += 2) { PG8_TRIP_HEAD(tt) PG8_TRIP_SP2(PG8_WAIT_V(8), PG8_MMA) }
	ds_read_b128 v[136:139], v134
	ds_read_b128 v[140:143], v134 offset:1024
	ds_read_b128 v[144:147], v134 offset:2048
	ds_read_b128 v[148:151], v134 offset:3072
	ds_read_b128 v[152:155], v135
	ds_read_b128 v[156:159], v135 offset:1024
	ds_read_b128 v[160:163], v135 offset:2048
	ds_read_b128 v[164:167], v135 offset:3072
	s_mov_b32 m0, s25
	ds_read_b128 v[168:171], v221 offset:32768
	ds_read_b128 v[172:175], v221 offset:33792
	ds_read_b128 v[176:179], v221 offset:34816
	ds_read_b128 v[180:183], v221 offset:35840
	ds_read_b128 v[184:187], v221 offset:36864
	ds_read_b128 v[188:191], v221 offset:37888
	ds_read_b128 v[202:205], v221 offset:38912
	ds_read_b128 v[206:209], v221 offset:39936
	s_add_u32 s70, s44, s82
	s_addc_u32 s71, s45, s83
	global_load_lds_dwordx4 v196, s[70:71]
	s_mov_b32 m0, s26
	s_nop 0
	s_add_u32 s70, s44, s56
	s_addc_u32 s71, s45, s57
	global_load_lds_dwordx4 v196, s[70:71]
	s_waitcnt vmcnt(8)
	s_waitcnt lgkmcnt(0)
	s_barrier
	v_mfma_f32_16x16x32_bf16 v[130:133], v[136:139], v[168:171], v[130:133]
	v_mfma_f32_16x16x32_bf16 v[130:133], v[140:143], v[172:175], v[130:133]
	v_mfma_f32_16x16x32_bf16 v[126:129], v[144:147], v[168:171], v[126:129]
	v_mfma_f32_16x16x32_bf16 v[126:129], v[148:151], v[172:175], v[126:129]
	v_mfma_f32_16x16x32_bf16 v[122:125], v[152:155], v[168:171], v[122:125]
	v_mfma_f32_16x16x32_bf16 v[122:125], v[156:159], v[172:175], v[122:125]
	v_mfma_f32_16x16x32_bf16 v[118:121], v[160:163], v[168:171], v[118:121]
	v_mfma_f32_16x16x32_bf16 v[118:121], v[164:167], v[172:175], v[118:121]
	v_mfma_f32_16x16x32_bf16 v[100:103], v[160:163], v[176:179], v[100:103]
	v_mfma_f32_16x16x32_bf16 v[100:103], v[164:167], v[180:183], v[100:103]
	v_mfma_f32_16x16x32_bf16 v[104:107], v[152:155], v[176:179], v[104:107]
	v_mfma_f32_16x16x32_bf16 v[104:107], v[156:159], v[180:183], v[104:107]
	v_mfma_f32_16x16x32_bf16 v[108:111], v[144:147], v[176:179], v[108:111]
	v_mfma_f32_16x16x32_bf16 v[108:111], v[148:151], v[180:183], v[108:111]
	v_mfma_f32_16x16x32_bf16 v[112:115], v[136:139], v[176:179], v[112:115]
	v_mfma_f32_16x16x32_bf16 v[112:115], v[140:143], v[180:183], v[112:115]
	v_mfma_f32_16x16x32_bf16 v[96:99], v[136:139], v[184:187], v[96:99]
	v_mfma_f32_16x16x32_bf16 v[96:99], v[140:143], v[188:191], v[96:99]
	v_mfma_f32_16x16x32_bf16 v[92:95], v[144:147], v[184:187], v[92:95]
	v_mfma_f32_16x16x32_bf16 v[92:95], v[148:151], v[188:191], v[92:95]
	v_mfma_f32_16x16x32_bf16 v[88:91], v[152:155], v[184:187], v[88:91]
	v_mfma_f32_16x16x32_bf16 v[88:91], v[156:159], v[188:191], v[88:91]
	v_mfma_f32_16x16x32_bf16 v[84:87], v[160:163], v[184:187], v[84:87]
	v_mfma_f32_16x16x32_bf16 v[84:87], v[164:167], v[188:191], v[84:87]
	v_mfma_f32_16x16x32_bf16 v[68:71], v[160:163], v[202:205], v[68:71]
	v_mfma_f32_16x16x32_bf16 v[68:71], v[164:167], v[206:209], v[68:71]
	v_mfma_f32_16x16x32_bf16 v[72:75], v[152:155], v[202:205], v[72:75]
	v_mfma_f32_16x16x32_bf16 v[72:75], v[156:159], v[206:209], v[72:75]
	v_mfma_f32_16x16x32_bf16 v[76:79], v[144:147], v[202:205], v[76:79]
	v_mfma_f32_16x16x32_bf16 v[76:79], v[148:151], v[206:209], v[76:79]
	v_mfma_f32_16x16x32_bf16 v[80:83], v[136:139], v[202:205], v[80:83]
	v_mfma_f32_16x16x32_bf16 v[80:83], v[140:143], v[206:209], v[80:83]
	s_barrier
	s_mov_b32 m0, s39
	ds_read_b128 v[168:171], v221 offset:49152
	ds_read_b128 v[172:175], v221 offset:50176
	ds_read_b128 v[176:179], v221 offset:51200
	ds_read_b128 v[180:183], v221 offset:52224
	ds_read_b128 v[184:187], v221 offset:53248
	ds_read_b128 v[188:191], v221 offset:54272
	ds_read_b128 v[202:205], v221 offset:55296
	ds_read_b128 v[206:209], v221 offset:56320
	s_add_u32 s70, s46, s78
	s_addc_u32 s71, s47, s79
	global_load_lds_dwordx4 v194, s[70:71]
	s_mov_b32 m0, s40
	s_nop 0
	s_add_u32 s70, s46, s84
	s_addc_u32 s71, s47, s85
	global_load_lds_dwordx4 v194, s[70:71]
	s_mov_b32 m0, s41
	s_add_u32 s70, s46, s50
	s_addc_u32 s71, s47, s51
	global_load_lds_dwordx4 v194, s[70:71]
	s_mov_b32 m0, s42
	s_nop 0
	s_add_u32 s70, s46, s54
	s_addc_u32 s71, s47, s55
	global_load_lds_dwordx4 v194, s[70:71]
	s_mov_b32 m0, s27
	s_nop 0
	s_add_u32 s70, s44, s78
	s_addc_u32 s71, s45, s79
	global_load_lds_dwordx4 v196, s[70:71]
	s_mov_b32 m0, s28
	s_nop 0
	s_add_u32 s70, s44, s92
	s_addc_u32 s71, s45, s93
	global_load_lds_dwordx4 v196, s[70:71]
	s_waitcnt vmcnt(8)
	s_waitcnt lgkmcnt(0)
	s_barrier
	v_mfma_f32_16x16x32_bf16 v[64:67], v[136:139], v[168:171], v[64:67]
	v_mfma_f32_16x16x32_bf16 v[64:67], v[140:143], v[172:175], v[64:67]
	v_mfma_f32_16x16x32_bf16 v[60:63], v[144:147], v[168:171], v[60:63]
	v_mfma_f32_16x16x32_bf16 v[60:63], v[148:151], v[172:175], v[60:63]
	v_mfma_f32_16x16x32_bf16 v[56:59], v[152:155], v[168:171], v[56:59]
	v_mfma_f32_16x16x32_bf16 v[56:59], v[156:159], v[172:175], v[56:59]
	v_mfma_f32_16x16x32_bf16 v[52:55], v[160:163], v[168:171], v[52:55]
	v_mfma_f32_16x16x32_bf16 v[52:55], v[164:167], v[172:175], v[52:55]
	v_mfma_f32_16x16x32_bf16 v[36:39], v[160:163], v[176:179], v[36:39]
	v_mfma_f32_16x16x32_bf16 v[36:39], v[164:167], v[180:183], v[36:39]
	v_mfma_f32_16x16x32_bf16 v[40:43], v[152:155], v[176:179], v[40:43]
	v_mfma_f32_16x16x32_bf16 v[40:43], v[156:159], v[180:183], v[40:43]
	v_mfma_f32_16x16x32_bf16 v[44:47], v[144:147], v[176:179], v[44:47]
	v_mfma_f32_16x16x32_bf16 v[44:47], v[148:151], v[180:183], v[44:47]
	v_mfma_f32_16x16x32_bf16 v[48:51], v[136:139], v[176:179], v[48:51]
	v_mfma_f32_16x16x32_bf16 v[48:51], v[140:143], v[180:183], v[48:51]
	v_mfma_f32_16x16x32_bf16 v[32:35], v[136:139], v[184:187], v[32:35]
	v_mfma_f32_16x16x32_bf16 v[32:35], v[140:143], v[188:191], v[32:35]
	v_mfma_f32_16x16x32_bf16 v[28:31], v[144:147], v[184:187], v[28:31]
	v_mfma_f32_16x16x32_bf16 v[28:31], v[148:151], v[188:191], v[28:31]
	v_mfma_f32_16x16x32_bf16 v[24:27], v[152:155], v[184:187], v[24:27]
	v_mfma_f32_16x16x32_bf16 v[24:27], v[156:159], v[188:191], v[24:27]
	v_mfma_f32_16x16x32_bf16 v[20:23], v[160:163], v[184:187], v[20:23]
	v_mfma_f32_16x16x32_bf16 v[20:23], v[164:167], v[188:191], v[20:23]
	v_mfma_f32_16x16x32_bf16 v[4:7], v[160:163], v[202:205], v[4:7]
	v_mfma_f32_16x16x32_bf16 v[4:7], v[164:167], v[206:209], v[4:7]
	v_mfma_f32_16x16x32_bf16 v[8:11], v[152:155], v[202:205], v[8:11]
	v_mfma_f32_16x16x32_bf16 v[8:11], v[156:159], v[206:209], v[8:11]
	v_mfma_f32_16x16x32_bf16 v[12:15], v[144:147], v[202:205], v[12:15]
	v_mfma_f32_16x16x32_bf16 v[12:15], v[148:151], v[206:209], v[12:15]
	v_mfma_f32_16x16x32_bf16 v[16:19], v[136:139], v[202:205], v[16:19]
	v_mfma_f32_16x16x32_bf16 v[16:19], v[140:143], v[206:209], v[16:19]
	s_barrier
	s_add_i32 s15, s15, 2
	s_add_u32 s20, s20, 0x100
	s_addc_u32 s21, s21, 0
	s_add_u32 s8, s8, 0x100
	s_addc_u32 s9, s9, 0
	s_cmp_gt_u32 s15, 29
	s_cbranch_scc0 .LBB0_594
	s_and_b64 vcc, exec, s[12:13]
	s_cbranch_vccz .LBB0_597
	s_barrier

.LBB0_700:
	ds_read_b128 v[120:123], v116
	ds_read_b128 v[132:135], v116 offset:1024
	ds_read_b128 v[144:147], v116 offset:2048
	ds_read_b128 v[148:151], v116 offset:3072
	ds_read_b128 v[152:155], v117
	ds_read_b128 v[156:159], v117 offset:1024
	ds_read_b128 v[166:169], v117 offset:2048
	ds_read_b128 v[170:173], v117 offset:3072
	s_add_u32 s27, s10, 0xfff7c080
	s_addc_u32 s47, s11, -1
	s_cmp_eq_u32 s26, 28
	s_cselect_b32 s49, s21, s47
	s_cselect_b32 s48, s20, s27
	s_cselect_b32 s51, s3, s25
	s_cselect_b32 s50, s4, s24
	s_mov_b32 m0, s5
	ds_read_b128 v[180:183], v178
	ds_read_b128 v[184:187], v178 offset:1024
	ds_read_b128 v[188:191], v178 offset:2048
	ds_read_b128 v[192:195], v178 offset:3072
	ds_read_b128 v[196:199], v178 offset:4096
	ds_read_b128 v[200:203], v178 offset:5120
	ds_read_b128 v[204:207], v178 offset:6144
	ds_read_b128 v[214:217], v178 offset:7168
	global_load_lds_dwordx4 v164, s[10:11]
	s_mov_b32 m0, s19
	s_nop 0
	s_add_u32 s70, s10, s96
	s_addc_u32 s71, s11, s97
	global_load_lds_dwordx4 v164, s[70:71]
	s_waitcnt vmcnt(8)
	s_waitcnt lgkmcnt(0)
	s_barrier
	v_mfma_f32_16x16x32_bf16 v[140:143], v[120:123], v[180:183], v[140:143]
	v_mfma_f32_16x16x32_bf16 v[140:143], v[132:135], v[184:187], v[140:143]
	v_mfma_f32_16x16x32_bf16 v[136:139], v[144:147], v[180:183], v[136:139]
	v_mfma_f32_16x16x32_bf16 v[136:139], v[148:151], v[184:187], v[136:139]
	v_mfma_f32_16x16x32_bf16 v[128:131], v[152:155], v[180:183], v[128:131]
	v_mfma_f32_16x16x32_bf16 v[128:131], v[156:159], v[184:187], v[128:131]
	v_mfma_f32_16x16x32_bf16 v[124:127], v[166:169], v[180:183], v[124:127]
	v_mfma_f32_16x16x32_bf16 v[124:127], v[170:173], v[184:187], v[124:127]
	v_mfma_f32_16x16x32_bf16 v[100:103], v[166:169], v[188:191], v[100:103]
	v_mfma_f32_16x16x32_bf16 v[100:103], v[170:173], v[192:195], v[100:103]
	v_mfma_f32_16x16x32_bf16 v[104:107], v[152:155], v[188:191], v[104:107]
	v_mfma_f32_16x16x32_bf16 v[104:107], v[156:159], v[192:195], v[104:107]
	v_mfma_f32_16x16x32_bf16 v[108:111], v[144:147], v[188:191], v[108:111]
	v_mfma_f32_16x16x32_bf16 v[108:111], v[148:151], v[192:195], v[108:111]
	v_mfma_f32_16x16x32_bf16 v[112:115], v[120:123], v[188:191], v[112:115]
	v_mfma_f32_16x16x32_bf16 v[112:115], v[132:135], v[192:195], v[112:115]
	v_mfma_f32_16x16x32_bf16 v[96:99], v[120:123], v[196:199], v[96:99]
	v_mfma_f32_16x16x32_bf16 v[96:99], v[132:135], v[200:203], v[96:99]
	v_mfma_f32_16x16x32_bf16 v[92:95], v[144:147], v[196:199], v[92:95]
	v_mfma_f32_16x16x32_bf16 v[92:95], v[148:151], v[200:203], v[92:95]
	v_mfma_f32_16x16x32_bf16 v[88:91], v[152:155], v[196:199], v[88:91]
	v_mfma_f32_16x16x32_bf16 v[88:91], v[156:159], v[200:203], v[88:91]
	v_mfma_f32_16x16x32_bf16 v[84:87], v[166:169], v[196:199], v[84:87]
	v_mfma_f32_16x16x32_bf16 v[84:87], v[170:173], v[200:203], v[84:87]
	v_mfma_f32_16x16x32_bf16 v[68:71], v[166:169], v[204:207], v[68:71]
	v_mfma_f32_16x16x32_bf16 v[68:71], v[170:173], v[214:217], v[68:71]
	v_mfma_f32_16x16x32_bf16 v[72:75], v[152:155], v[204:207], v[72:75]
	v_mfma_f32_16x16x32_bf16 v[72:75], v[156:159], v[214:217], v[72:75]
	v_mfma_f32_16x16x32_bf16 v[76:79], v[144:147], v[204:207], v[76:79]
	v_mfma_f32_16x16x32_bf16 v[76:79], v[148:151], v[214:217], v[76:79]
	v_mfma_f32_16x16x32_bf16 v[80:83], v[120:123], v[204:207], v[80:83]
	v_mfma_f32_16x16x32_bf16 v[80:83], v[132:135], v[214:217], v[80:83]
	s_barrier
	s_mov_b32 m0, s33
	ds_read_b128 v[180:183], v178 offset:16384
	ds_read_b128 v[184:187], v178 offset:17408
	ds_read_b128 v[188:191], v178 offset:18432
	ds_read_b128 v[192:195], v178 offset:19456
	ds_read_b128 v[196:199], v178 offset:20480
	ds_read_b128 v[200:203], v178 offset:21504
	ds_read_b128 v[204:207], v178 offset:22528
	ds_read_b128 v[214:217], v178 offset:23552
	global_load_lds_dwordx4 v160, s[50:51]
	s_mov_b32 m0, s40
	s_nop 0
	s_add_u32 s70, s50, s90
	s_addc_u32 s71, s51, s91
	global_load_lds_dwordx4 v160, s[70:71]
	s_mov_b32 m0, s41
	s_nop 0
	s_add_u32 s70, s50, s52
	s_addc_u32 s71, s51, s53
	global_load_lds_dwordx4 v160, s[70:71]
	s_mov_b32 m0, s42
	s_nop 0
	s_add_u32 s70, s50, s56
	s_addc_u32 s71, s51, s57
	global_load_lds_dwordx4 v160, s[70:71]
	s_mov_b32 m0, s29
	s_nop 0
	global_load_lds_dwordx4 v162, s[48:49]
	s_mov_b32 m0, s30
	s_nop 0
	s_add_u32 s70, s48, s96
	s_addc_u32 s71, s49, s97
	global_load_lds_dwordx4 v162, s[70:71]
	s_waitcnt vmcnt(8)
	s_waitcnt lgkmcnt(0)
	s_barrier
	v_mfma_f32_16x16x32_bf16 v[56:59], v[120:123], v[180:183], v[56:59]
	v_mfma_f32_16x16x32_bf16 v[56:59], v[132:135], v[184:187], v[56:59]
	v_mfma_f32_16x16x32_bf16 v[52:55], v[144:147], v[180:183], v[52:55]
	v_mfma_f32_16x16x32_bf16 v[52:55], v[148:151], v[184:187], v[52:55]
	v_mfma_f32_16x16x32_bf16 v[64:67], v[152:155], v[180:183], v[64:67]
	v_mfma_f32_16x16x32_bf16 v[64:67], v[156:159], v[184:187], v[64:67]
	v_mfma_f32_16x16x32_bf16 v[60:63], v[166:169], v[180:183], v[60:63]
	v_mfma_f32_16x16x32_bf16 v[60:63], v[170:173], v[184:187], v[60:63]
	v_mfma_f32_16x16x32_bf16 v[36:39], v[166:169], v[188:191], v[36:39]
	v_mfma_f32_16x16x32_bf16 v[36:39], v[170:173], v[192:195], v[36:39]
	v_mfma_f32_16x16x32_bf16 v[40:43], v[152:155], v[188:191], v[40:43]
	v_mfma_f32_16x16x32_bf16 v[40:43], v[156:159], v[192:195], v[40:43]
	v_mfma_f32_16x16x32_bf16 v[44:47], v[144:147], v[188:191], v[44:47]
	v_mfma_f32_16x16x32_bf16 v[44:47], v[148:151], v[192:195], v[44:47]
	v_mfma_f32_16x16x32_bf16 v[48:51], v[120:123], v[188:191], v[48:51]
	v_mfma_f32_16x16x32_bf16 v[48:51], v[132:135], v[192:195], v[48:51]
	v_mfma_f32_16x16x32_bf16 v[32:35], v[120:123], v[196:199], v[32:35]
	v_mfma_f32_16x16x32_bf16 v[32:35], v[132:135], v[200:203], v[32:35]
	v_mfma_f32_16x16x32_bf16 v[28:31], v[144:147], v[196:199], v[28:31]
	v_mfma_f32_16x16x32_bf16 v[28:31], v[148:151], v[200:203], v[28:31]
	v_mfma_f32_16x16x32_bf16 v[24:27], v[152:155], v[196:199], v[24:27]
	v_mfma_f32_16x16x32_bf16 v[24:27], v[156:159], v[200:203], v[24:27]
	v_mfma_f32_16x16x32_bf16 v[20:23], v[166:169], v[196:199], v[20:23]
	v_mfma_f32_16x16x32_bf16 v[20:23], v[170:173], v[200:203], v[20:23]
	v_mfma_f32_16x16x32_bf16 v[4:7], v[166:169], v[204:207], v[4:7]
	v_mfma_f32_16x16x32_bf16 v[4:7], v[170:173], v[214:217], v[4:7]
	v_mfma_f32_16x16x32_bf16 v[8:11], v[152:155], v[204:207], v[8:11]
	v_mfma_f32_16x16x32_bf16 v[8:11], v[156:159], v[214:217], v[8:11]
	v_mfma_f32_16x16x32_bf16 v[12:15], v[144:147], v[204:207], v[12:15]
	v_mfma_f32_16x16x32_bf16 v[12:15], v[148:151], v[214:217], v[12:15]
	v_mfma_f32_16x16x32_bf16 v[16:19], v[120:123], v[204:207], v[16:19]
	v_mfma_f32_16x16x32_bf16 v[16:19], v[132:135], v[214:217], v[16:19]
	s_barrier
; #define PG8_MMA(ai, bj, At, Bt) do { __builtin_amdgcn_s_setprio(1); _Pragma("unroll") for (int m = 0; m < 4; ++m) _Pragma("unroll") for (int n = 0; n < 2; ++n) _Pragma("unroll") for (int k = 0; k < 2; ++k) \
;         acc[ai][bj][m][n] = __builtin_amdgcn_mfma_f32_16x16x32_bf16(Bt[n][k], At[m][k], acc[ai][bj][m][n], 0, 0, 0); __builtin_amdgcn_s_setprio(0); } while (0)
; #define PG8_WAIT_V(n) asm volatile("s_waitcnt vmcnt(" #n ")" ::: "memory")
; #define PG8_TRIP_HEAD(T) const int t = (T); const bool last = (t == nt - 2); \
;             const char* a1 = cA + (size_t)(t + 1) * kstep; \
;             const char* a2 = last ? nA : cA + (size_t)(t + 2) * kstep; const char* b2 = last ? nB : cB + (size_t)(t + 2) * kstep; \
;             const char* a3 = a2 + kstep; const char* b3 = b2 + kstep; \
;             if (last && has_next) S.a_ready(nxt);
; template <class Epi, class Sched, bool ALIGN_EPI = false, bool SP2 = false>
; __device__ __forceinline__ void gemm_phase(PG8_LAS unsigned char* lds, const Gemm g, const Sched& S, const Epi& E) {
;     ...
;         if constexpr (SP2) {
;             { PG8_TRIP_HEAD(0) PG8_TRIP_SP2(asm volatile("s_waitcnt vmcnt(%0)" :: "n"(8 + Epi::NST) : "memory"), PG8_MMAZ) }
;             for (int tt = 2; tt < nt; tt += 2) { PG8_TRIP_HEAD(tt) PG8_TRIP_SP2(PG8_WAIT_V(8), PG8_MMA) }
	ds_read_b128 v[120:123], v118
	ds_read_b128 v[132:135], v118 offset:1024
	ds_read_b128 v[144:147], v118 offset:2048
	ds_read_b128 v[148:151], v118 offset:3072
	ds_read_b128 v[152:155], v119
	ds_read_b128 v[156:159], v119 offset:1024
	ds_read_b128 v[166:169], v119 offset:2048
	ds_read_b128 v[170:173], v119 offset:3072
	s_mov_b32 m0, s31
	ds_read_b128 v[180:183], v178 offset:32768
	ds_read_b128 v[184:187], v178 offset:33792
	ds_read_b128 v[188:191], v178 offset:34816
	ds_read_b128 v[192:195], v178 offset:35840
	ds_read_b128 v[196:199], v178 offset:36864
	ds_read_b128 v[200:203], v178 offset:37888
	ds_read_b128 v[204:207], v178 offset:38912
	ds_read_b128 v[214:217], v178 offset:39936
	s_add_u32 s70, s48, s82
	s_addc_u32 s71, s49, s83
	global_load_lds_dwordx4 v162, s[70:71]
	s_mov_b32 m0, s34
	s_nop 0
	s_add_u32 s70, s48, s62
	s_addc_u32 s71, s49, s63
	global_load_lds_dwordx4 v162, s[70:71]
	s_waitcnt vmcnt(8)
	s_waitcnt lgkmcnt(0)
	s_barrier
	v_mfma_f32_16x16x32_bf16 v[140:143], v[120:123], v[180:183], v[140:143]
	v_mfma_f32_16x16x32_bf16 v[140:143], v[132:135], v[184:187], v[140:143]
	v_mfma_f32_16x16x32_bf16 v[136:139], v[144:147], v[180:183], v[136:139]
	v_mfma_f32_16x16x32_bf16 v[136:139], v[148:151], v[184:187], v[136:139]
	v_mfma_f32_16x16x32_bf16 v[128:131], v[152:155], v[180:183], v[128:131]
	v_mfma_f32_16x16x32_bf16 v[128:131], v[156:159], v[184:187], v[128:131]
	v_mfma_f32_16x16x32_bf16 v[124:127], v[166:169], v[180:183], v[124:127]
	v_mfma_f32_16x16x32_bf16 v[124:127], v[170:173], v[184:187], v[124:127]
	v_mfma_f32_16x16x32_bf16 v[100:103], v[166:169], v[188:191], v[100:103]
	v_mfma_f32_16x16x32_bf16 v[100:103], v[170:173], v[192:195], v[100:103]
	v_mfma_f32_16x16x32_bf16 v[104:107], v[152:155], v[188:191], v[104:107]
	v_mfma_f32_16x16x32_bf16 v[104:107], v[156:159], v[192:195], v[104:107]
	v_mfma_f32_16x16x32_bf16 v[108:111], v[144:147], v[188:191], v[108:111]
	v_mfma_f32_16x16x32_bf16 v[108:111], v[148:151], v[192:195], v[108:111]
	v_mfma_f32_16x16x32_bf16 v[112:115], v[120:123], v[188:191], v[112:115]
	v_mfma_f32_16x16x32_bf16 v[112:115], v[132:135], v[192:195], v[112:115]
	v_mfma_f32_16x16x32_bf16 v[96:99], v[120:123], v[196:199], v[96:99]
	v_mfma_f32_16x16x32_bf16 v[96:99], v[132:135], v[200:203], v[96:99]
	v_mfma_f32_16x16x32_bf16 v[92:95], v[144:147], v[196:199], v[92:95]
	v_mfma_f32_16x16x32_bf16 v[92:95], v[148:151], v[200:203], v[92:95]
	v_mfma_f32_16x16x32_bf16 v[88:91], v[152:155], v[196:199], v[88:91]
	v_mfma_f32_16x16x32_bf16 v[88:91], v[156:159], v[200:203], v[88:91]
	v_mfma_f32_16x16x32_bf16 v[84:87], v[166:169], v[196:199], v[84:87]
	v_mfma_f32_16x16x32_bf16 v[84:87], v[170:173], v[200:203], v[84:87]
	v_mfma_f32_16x16x32_bf16 v[68:71], v[166:169], v[204:207], v[68:71]
	v_mfma_f32_16x16x32_bf16 v[68:71], v[170:173], v[214:217], v[68:71]
	v_mfma_f32_16x16x32_bf16 v[72:75], v[152:155], v[204:207], v[72:75]
	v_mfma_f32_16x16x32_bf16 v[72:75], v[156:159], v[214:217], v[72:75]
	v_mfma_f32_16x16x32_bf16 v[76:79], v[144:147], v[204:207], v[76:79]
	v_mfma_f32_16x16x32_bf16 v[76:79], v[148:151], v[214:217], v[76:79]
	v_mfma_f32_16x16x32_bf16 v[80:83], v[120:123], v[204:207], v[80:83]
	v_mfma_f32_16x16x32_bf16 v[80:83], v[132:135], v[214:217], v[80:83]
	s_barrier
	s_mov_b32 m0, s43
	ds_read_b128 v[180:183], v178 offset:49152
	ds_read_b128 v[184:187], v178 offset:50176
	ds_read_b128 v[188:191], v178 offset:51200
	ds_read_b128 v[192:195], v178 offset:52224
	ds_read_b128 v[196:199], v178 offset:53248
	ds_read_b128 v[200:203], v178 offset:54272
	ds_read_b128 v[204:207], v178 offset:55296
	ds_read_b128 v[214:217], v178 offset:56320
	s_add_u32 s70, s50, s78
	s_addc_u32 s71, s51, s79
	global_load_lds_dwordx4 v160, s[70:71]
	s_mov_b32 m0, s44
	s_nop 0
	s_add_u32 s70, s50, s84
	s_addc_u32 s71, s51, s85
	global_load_lds_dwordx4 v160, s[70:71]
	s_mov_b32 m0, s45
	s_add_u32 s70, s50, s54
	s_addc_u32 s71, s51, s55
	global_load_lds_dwordx4 v160, s[70:71]
	s_mov_b32 m0, s46
	s_nop 0
	s_add_u32 s70, s50, s60
	s_addc_u32 s71, s51, s61
	global_load_lds_dwordx4 v160, s[70:71]
	s_mov_b32 m0, s36
	s_nop 0
	s_add_u32 s70, s48, s78
	s_addc_u32 s71, s49, s79
	global_load_lds_dwordx4 v162, s[70:71]
	s_mov_b32 m0, s37
	s_nop 0
	s_add_u32 s70, s48, s92
	s_addc_u32 s71, s49, s93
	global_load_lds_dwordx4 v162, s[70:71]
	s_waitcnt vmcnt(8)
	s_waitcnt lgkmcnt(0)
	s_barrier
	v_mfma_f32_16x16x32_bf16 v[56:59], v[120:123], v[180:183], v[56:59]
	v_mfma_f32_16x16x32_bf16 v[56:59], v[132:135], v[184:187], v[56:59]
	v_mfma_f32_16x16x32_bf16 v[52:55], v[144:147], v[180:183], v[52:55]
	v_mfma_f32_16x16x32_bf16 v[52:55], v[148:151], v[184:187], v[52:55]
	v_mfma_f32_16x16x32_bf16 v[64:67], v[152:155], v[180:183], v[64:67]
	v_mfma_f32_16x16x32_bf16 v[64:67], v[156:159], v[184:187], v[64:67]
	v_mfma_f32_16x16x32_bf16 v[60:63], v[166:169], v[180:183], v[60:63]
	v_mfma_f32_16x16x32_bf16 v[60:63], v[170:173], v[184:187], v[60:63]
	v_mfma_f32_16x16x32_bf16 v[36:39], v[166:169], v[188:191], v[36:39]
	v_mfma_f32_16x16x32_bf16 v[36:39], v[170:173], v[192:195], v[36:39]
	v_mfma_f32_16x16x32_bf16 v[40:43], v[152:155], v[188:191], v[40:43]
	v_mfma_f32_16x16x32_bf16 v[40:43], v[156:159], v[192:195], v[40:43]
	v_mfma_f32_16x16x32_bf16 v[44:47], v[144:147], v[188:191], v[44:47]
	v_mfma_f32_16x16x32_bf16 v[44:47], v[148:151], v[192:195], v[44:47]
	v_mfma_f32_16x16x32_bf16 v[48:51], v[120:123], v[188:191], v[48:51]
	v_mfma_f32_16x16x32_bf16 v[48:51], v[132:135], v[192:195], v[48:51]
	v_mfma_f32_16x16x32_bf16 v[32:35], v[120:123], v[196:199], v[32:35]
	v_mfma_f32_16x16x32_bf16 v[32:35], v[132:135], v[200:203], v[32:35]
	v_mfma_f32_16x16x32_bf16 v[28:31], v[144:147], v[196:199], v[28:31]
	v_mfma_f32_16x16x32_bf16 v[28:31], v[148:151], v[200:203], v[28:31]
	v_mfma_f32_16x16x32_bf16 v[24:27], v[152:155], v[196:199], v[24:27]
	v_mfma_f32_16x16x32_bf16 v[24:27], v[156:159], v[200:203], v[24:27]
	v_mfma_f32_16x16x32_bf16 v[20:23], v[166:169], v[196:199], v[20:23]
	v_mfma_f32_16x16x32_bf16 v[20:23], v[170:173], v[200:203], v[20:23]
	v_mfma_f32_16x16x32_bf16 v[4:7], v[166:169], v[204:207], v[4:7]
	v_mfma_f32_16x16x32_bf16 v[4:7], v[170:173], v[214:217], v[4:7]
	v_mfma_f32_16x16x32_bf16 v[8:11], v[152:155], v[204:207], v[8:11]
	v_mfma_f32_16x16x32_bf16 v[8:11], v[156:159], v[214:217], v[8:11]
	v_mfma_f32_16x16x32_bf16 v[12:15], v[144:147], v[204:207], v[12:15]
	v_mfma_f32_16x16x32_bf16 v[12:15], v[148:151], v[214:217], v[12:15]
	v_mfma_f32_16x16x32_bf16 v[16:19], v[120:123], v[204:207], v[16:19]
	v_mfma_f32_16x16x32_bf16 v[16:19], v[132:135], v[214:217], v[16:19]
	s_barrier
	s_add_i32 s26, s26, 2
	s_add_u32 s10, s10, 0x100
	s_addc_u32 s11, s11, 0
	s_add_u32 s24, s24, 0x100
	s_addc_u32 s25, s25, 0
	s_cmp_gt_u32 s26, 29
	s_cbranch_scc0 .LBB0_700
	s_and_b64 vcc, exec, s[16:17]
	s_cbranch_vccz .LBB0_703
	s_barrier
